# E6 plus 64-byte alignment of all hot inner-loop headers (.p2align 6)
# baseline (speedup 1.0000x reference)
.LBB0_65:
	ds_read2_b32 v[214:215], v140 offset1:32
	s_andn2_b64 vcc, exec, s[12:13]
	s_mov_b32 s20, s62
	s_waitcnt vmcnt(0) lgkmcnt(0)
	v_mul_f32_e32 v77, v68, v214
	ds_read_b32 v210, v152
	ds_read_b32 v211, v162
	ds_read_b32 v212, v170
	ds_read_b32 v213, v178
	ds_read_b32 v214, v186
	ds_read_b32 v216, v194
	ds_read_b32 v217, v202
	ds_read_b32 v218, v142
	s_waitcnt lgkmcnt(7)
	v_mul_f32_e32 v210, v69, v210
	v_cvt_pk_bf16_f32 v210, v77, v210
	s_waitcnt lgkmcnt(6)
	v_mul_f32_e32 v77, v70, v211
	s_waitcnt lgkmcnt(5)
	v_mul_f32_e32 v211, v71, v212
	v_cvt_pk_bf16_f32 v211, v77, v211
	s_waitcnt lgkmcnt(4)
	v_mul_f32_e32 v77, v64, v213
	s_waitcnt lgkmcnt(3)
	v_mul_f32_e32 v212, v65, v214
	v_cvt_pk_bf16_f32 v212, v77, v212
	s_waitcnt lgkmcnt(2)
	v_mul_f32_e32 v77, v66, v216
	s_waitcnt lgkmcnt(1)
	v_mul_f32_e32 v213, v67, v217
	v_cvt_pk_bf16_f32 v213, v77, v213
	v_add_u32_e32 v77, s43, v139
	v_mad_i64_i32 v[216:217], s[6:7], s42, v77, 0
	v_lshl_add_u64 v[216:217], v[216:217], 1, s[4:5]
	s_lshl_b64 s[6:7], s[8:9], 1
	v_lshl_add_u64 v[216:217], v[216:217], 0, s[6:7]
	v_lshl_add_u64 v[216:217], v[216:217], 0, v[72:73]
	global_store_dwordx4 v[216:217], v[210:213], off
	s_waitcnt lgkmcnt(0)
	v_mul_f32_e32 v77, v68, v218
	ds_read_b32 v210, v153
	ds_read_b32 v211, v163
	ds_read_b32 v212, v171
	ds_read_b32 v213, v179
	ds_read_b32 v214, v187
	ds_read_b32 v216, v195
	ds_read_b32 v217, v203
	ds_read_b32 v218, v144
	s_waitcnt lgkmcnt(7)
	v_mul_f32_e32 v210, v69, v210
	v_cvt_pk_bf16_f32 v210, v77, v210
	s_waitcnt lgkmcnt(6)
	v_mul_f32_e32 v77, v70, v211
	s_waitcnt lgkmcnt(5)
	v_mul_f32_e32 v211, v71, v212
	v_cvt_pk_bf16_f32 v211, v77, v211
	s_waitcnt lgkmcnt(4)
	v_mul_f32_e32 v77, v64, v213
	s_waitcnt lgkmcnt(3)
	v_mul_f32_e32 v212, v65, v214
	v_cvt_pk_bf16_f32 v212, v77, v212
	s_waitcnt lgkmcnt(2)
	v_mul_f32_e32 v77, v66, v216
	s_waitcnt lgkmcnt(1)
	v_mul_f32_e32 v213, v67, v217
	v_cvt_pk_bf16_f32 v213, v77, v213
	v_add_u32_e32 v77, s43, v141
	v_mad_i64_i32 v[216:217], s[8:9], s42, v77, 0
	v_lshl_add_u64 v[216:217], v[216:217], 1, s[4:5]
	v_lshl_add_u64 v[216:217], v[216:217], 0, s[6:7]
	v_lshl_add_u64 v[216:217], v[216:217], 0, v[72:73]
	global_store_dwordx4 v[216:217], v[210:213], off
	s_waitcnt lgkmcnt(0)
	v_mul_f32_e32 v77, v68, v218
	ds_read_b32 v210, v154
	ds_read_b32 v211, v164
	ds_read_b32 v212, v172
	ds_read_b32 v213, v180
	ds_read_b32 v214, v188
	ds_read_b32 v216, v196
	ds_read_b32 v217, v204
	ds_read_b32 v218, v145
	s_waitcnt lgkmcnt(7)
	v_mul_f32_e32 v210, v69, v210
	v_cvt_pk_bf16_f32 v210, v77, v210
	s_waitcnt lgkmcnt(6)
	v_mul_f32_e32 v77, v70, v211
	s_waitcnt lgkmcnt(5)
	v_mul_f32_e32 v211, v71, v212
	v_cvt_pk_bf16_f32 v211, v77, v211
	s_waitcnt lgkmcnt(4)
	v_mul_f32_e32 v77, v64, v213
	s_waitcnt lgkmcnt(3)
	v_mul_f32_e32 v212, v65, v214
	v_cvt_pk_bf16_f32 v212, v77, v212
	s_waitcnt lgkmcnt(2)
	v_mul_f32_e32 v77, v66, v216
	s_waitcnt lgkmcnt(1)
	v_mul_f32_e32 v213, v67, v217
	v_cvt_pk_bf16_f32 v213, v77, v213
	v_add_u32_e32 v77, s43, v143
	v_mad_i64_i32 v[216:217], s[8:9], s42, v77, 0
	v_lshl_add_u64 v[216:217], v[216:217], 1, s[4:5]
	v_lshl_add_u64 v[216:217], v[216:217], 0, s[6:7]
	v_lshl_add_u64 v[216:217], v[216:217], 0, v[72:73]
	global_store_dwordx4 v[216:217], v[210:213], off
	s_waitcnt lgkmcnt(0)
	v_mul_f32_e32 v77, v68, v218
	ds_read_b32 v210, v156
	ds_read_b32 v211, v165
	ds_read_b32 v212, v173
	ds_read_b32 v213, v181
	ds_read_b32 v214, v189
	ds_read_b32 v216, v197
	ds_read_b32 v217, v205
	ds_read_b32 v218, v158
	s_waitcnt lgkmcnt(7)
	v_mul_f32_e32 v210, v69, v210
	v_cvt_pk_bf16_f32 v210, v77, v210
	s_waitcnt lgkmcnt(6)
	v_mul_f32_e32 v77, v70, v211
	s_waitcnt lgkmcnt(5)
	v_mul_f32_e32 v211, v71, v212
	v_cvt_pk_bf16_f32 v211, v77, v211
	s_waitcnt lgkmcnt(4)
	v_mul_f32_e32 v77, v64, v213
	s_waitcnt lgkmcnt(3)
	v_mul_f32_e32 v212, v65, v214
	v_cvt_pk_bf16_f32 v212, v77, v212
	s_waitcnt lgkmcnt(2)
	v_mul_f32_e32 v77, v66, v216
	s_waitcnt lgkmcnt(1)
	v_mul_f32_e32 v213, v67, v217
	v_cvt_pk_bf16_f32 v213, v77, v213
	v_add_u32_e32 v77, s43, v155
	v_mad_i64_i32 v[216:217], s[8:9], s42, v77, 0
	v_lshl_add_u64 v[216:217], v[216:217], 1, s[4:5]
	v_lshl_add_u64 v[216:217], v[216:217], 0, s[6:7]
	v_lshl_add_u64 v[216:217], v[216:217], 0, v[72:73]
	global_store_dwordx4 v[216:217], v[210:213], off
	v_mul_f32_e32 v77, v68, v215
	s_waitcnt lgkmcnt(0)
	v_mul_f32_e32 v210, v69, v218
	v_cvt_pk_bf16_f32 v210, v77, v210
	ds_read_b32 v77, v166
	ds_read_b32 v211, v174
	ds_read_b32 v212, v182
	ds_read_b32 v213, v190
	ds_read_b32 v214, v198
	ds_read_b32 v215, v206
	ds_read_b32 v216, v147
	ds_read_b32 v217, v159
	s_waitcnt lgkmcnt(7)
	v_mul_f32_e32 v77, v70, v77
	s_waitcnt lgkmcnt(6)
	v_mul_f32_e32 v211, v71, v211
	v_cvt_pk_bf16_f32 v211, v77, v211
	s_waitcnt lgkmcnt(5)
	v_mul_f32_e32 v77, v64, v212
	s_waitcnt lgkmcnt(4)
	v_mul_f32_e32 v212, v65, v213
	v_cvt_pk_bf16_f32 v212, v77, v212
	s_waitcnt lgkmcnt(3)
	v_mul_f32_e32 v77, v66, v214
	s_waitcnt lgkmcnt(2)
	v_mul_f32_e32 v213, v67, v215
	v_cvt_pk_bf16_f32 v213, v77, v213
	v_add_u32_e32 v77, s43, v157
	v_mad_i64_i32 v[214:215], s[8:9], s42, v77, 0
	v_lshl_add_u64 v[214:215], v[214:215], 1, s[4:5]
	v_lshl_add_u64 v[214:215], v[214:215], 0, s[6:7]
	v_lshl_add_u64 v[214:215], v[214:215], 0, v[72:73]
	global_store_dwordx4 v[214:215], v[210:213], off
	s_waitcnt lgkmcnt(1)
	v_mul_f32_e32 v77, v68, v216
	s_waitcnt lgkmcnt(0)
	v_mul_f32_e32 v210, v69, v217
	v_cvt_pk_bf16_f32 v210, v77, v210
	ds_read_b32 v77, v167
	ds_read_b32 v211, v175
	ds_read_b32 v212, v183
	ds_read_b32 v213, v191
	ds_read_b32 v214, v199
	ds_read_b32 v215, v207
	ds_read_b32 v216, v149
	ds_read_b32 v217, v160
	s_waitcnt lgkmcnt(7)
	v_mul_f32_e32 v77, v70, v77
	s_waitcnt lgkmcnt(6)
	v_mul_f32_e32 v211, v71, v211
	v_cvt_pk_bf16_f32 v211, v77, v211
	s_waitcnt lgkmcnt(5)
	v_mul_f32_e32 v77, v64, v212
	s_waitcnt lgkmcnt(4)
	v_mul_f32_e32 v212, v65, v213
	v_cvt_pk_bf16_f32 v212, v77, v212
	s_waitcnt lgkmcnt(3)
	v_mul_f32_e32 v77, v66, v214
	s_waitcnt lgkmcnt(2)
	v_mul_f32_e32 v213, v67, v215
	v_cvt_pk_bf16_f32 v213, v77, v213
	v_add_u32_e32 v77, s43, v146
	v_mad_i64_i32 v[214:215], s[8:9], s42, v77, 0
	v_lshl_add_u64 v[214:215], v[214:215], 1, s[4:5]
	v_lshl_add_u64 v[214:215], v[214:215], 0, s[6:7]
	v_lshl_add_u64 v[214:215], v[214:215], 0, v[72:73]
	global_store_dwordx4 v[214:215], v[210:213], off
	s_waitcnt lgkmcnt(1)
	v_mul_f32_e32 v77, v68, v216
	s_waitcnt lgkmcnt(0)
	v_mul_f32_e32 v210, v69, v217
	v_cvt_pk_bf16_f32 v210, v77, v210
	ds_read_b32 v77, v168
	ds_read_b32 v211, v176
	ds_read_b32 v212, v184
	ds_read_b32 v213, v192
	ds_read_b32 v214, v200
	ds_read_b32 v215, v208
	ds_read_b32 v216, v151
	ds_read_b32 v217, v161
	s_waitcnt lgkmcnt(7)
	v_mul_f32_e32 v77, v70, v77
	s_waitcnt lgkmcnt(6)
	v_mul_f32_e32 v211, v71, v211
	v_cvt_pk_bf16_f32 v211, v77, v211
	s_waitcnt lgkmcnt(5)
	v_mul_f32_e32 v77, v64, v212
	s_waitcnt lgkmcnt(4)
	v_mul_f32_e32 v212, v65, v213
	v_cvt_pk_bf16_f32 v212, v77, v212
	s_waitcnt lgkmcnt(3)
	v_mul_f32_e32 v77, v66, v214
	s_waitcnt lgkmcnt(2)
	v_mul_f32_e32 v213, v67, v215
	v_cvt_pk_bf16_f32 v213, v77, v213
	v_add_u32_e32 v77, s43, v148
	v_mad_i64_i32 v[214:215], s[8:9], s42, v77, 0
	v_lshl_add_u64 v[214:215], v[214:215], 1, s[4:5]
	v_lshl_add_u64 v[214:215], v[214:215], 0, s[6:7]
	v_lshl_add_u64 v[214:215], v[214:215], 0, v[72:73]
	global_store_dwordx4 v[214:215], v[210:213], off
	ds_read_b32 v77, v169
	ds_read_b32 v210, v177
	ds_read_b32 v211, v185
	ds_read_b32 v212, v193
	ds_read_b32 v213, v201
	ds_read_b32 v214, v209
	s_waitcnt lgkmcnt(7)
	v_mul_f32_e32 v68, v68, v216
	s_waitcnt lgkmcnt(6)
	v_mul_f32_e32 v69, v69, v217
	v_cvt_pk_bf16_f32 v68, v68, v69
	s_waitcnt lgkmcnt(5)
	v_mul_f32_e32 v69, v70, v77
	s_waitcnt lgkmcnt(4)
	v_mul_f32_e32 v70, v71, v210
	s_waitcnt lgkmcnt(3)
	v_mul_f32_e32 v64, v64, v211
	v_cvt_pk_bf16_f32 v69, v69, v70
	s_waitcnt lgkmcnt(2)
	v_mul_f32_e32 v65, v65, v212
	v_cvt_pk_bf16_f32 v70, v64, v65
	s_waitcnt lgkmcnt(1)
	v_mul_f32_e32 v64, v66, v213
	s_waitcnt lgkmcnt(0)
	v_mul_f32_e32 v65, v67, v214
	v_cvt_pk_bf16_f32 v71, v64, v65
	v_add_u32_e32 v64, s43, v150
	v_mad_i64_i32 v[64:65], s[8:9], s42, v64, 0
	v_lshl_add_u64 v[64:65], v[64:65], 1, s[4:5]
	v_lshl_add_u64 v[64:65], v[64:65], 0, s[6:7]
	v_lshl_add_u64 v[64:65], v[64:65], 0, v[72:73]
	global_store_dwordx4 v[64:65], v[68:71], off
	s_waitcnt lgkmcnt(0)
	s_mov_b32 s43, s26
	s_mov_b64 s[4:5], s[14:15]
	s_mov_b64 s[6:7], s[16:17]
	s_mov_b32 s42, s63
	s_mov_b32 s8, s21
	s_cbranch_vccz .LBB0_99
	.p2align 6

.LBB0_101:
	s_or_b64 exec, exec, s[20:21]
	v_lshlrev_b64 v[6:7], 19, v[6:7]
	v_lshl_add_u64 v[6:7], s[14:15], 0, v[6:7]
	v_lshlrev_b32_e32 v4, 11, v12
	v_add_u32_e32 v11, s23, v11
	v_lshl_add_u64 v[6:7], v[6:7], 0, v[4:5]
	v_lshlrev_b32_e32 v4, 1, v13
	v_cmp_lt_i32_e32 vcc, s26, v11
	v_lshl_add_u64 v[6:7], v[6:7], 0, v[4:5]
	s_or_b64 s[16:17], vcc, s[16:17]
	v_add_u32_e32 v10, s24, v10
	global_store_dwordx4 v[6:7], v[0:3], off
	s_andn2_b64 exec, exec, s[16:17]
	s_cbranch_execz .LBB0_104
	.p2align 6

.LBB0_104:
	s_or_b64 exec, exec, s[12:13]
	s_movk_i32 s4, 0x4000
	v_cmp_gt_i32_e32 vcc, s4, v8
	s_and_saveexec_b64 s[4:5], vcc
	s_cbranch_execz .LBB0_107
	s_add_u32 s6, s30, 0x1200000
	v_mov_b32_e32 v1, 0
	s_addc_u32 s7, s31, 0
	s_lshl_b32 s12, s29, 12
	s_mov_b64 s[8:9], 0
	v_mov_b32_e32 v2, 0x2c0
	v_mov_b32_e32 v4, v1
	v_mov_b32_e32 v5, v1
	v_mov_b32_e32 v6, v1
	v_mov_b32_e32 v7, v1
	s_movk_i32 s13, 0x3fff
	.p2align 6

.LBB0_179:
	s_or_b64 exec, exec, s[22:23]
	s_add_i32 s12, s12, s14
	s_add_u32 s25, s25, s16
	s_addc_u32 s26, s26, s17
	v_lshl_add_u64 v[0:1], v[0:1], 0, s[18:19]
	s_cmp_lt_i32 s12, 0x8000
	v_lshl_add_u64 v[4:5], v[4:5], 0, s[20:21]
	s_cbranch_scc0 .LBB0_182
	.p2align 6

.LBB0_258:
	s_add_u32 s21, s36, 0x100
	v_mov_b32_e32 v0, 0
	s_addc_u32 s23, s37, 0
	s_mov_b32 s29, -2
	v_mov_b32_e32 v1, v0
	v_mov_b32_e32 v2, v0
	v_mov_b32_e32 v3, v0
	v_mov_b32_e32 v4, v0
	v_mov_b32_e32 v5, v0
	v_mov_b32_e32 v6, v0
	v_mov_b32_e32 v7, v0
	v_mov_b32_e32 v12, v0
	v_mov_b32_e32 v13, v0
	v_mov_b32_e32 v14, v0
	v_mov_b32_e32 v15, v0
	v_mov_b32_e32 v20, v0
	v_mov_b32_e32 v21, v0
	v_mov_b32_e32 v22, v0
	v_mov_b32_e32 v23, v0
	v_mov_b32_e32 v28, v0
	v_mov_b32_e32 v29, v0
	v_mov_b32_e32 v30, v0
	v_mov_b32_e32 v31, v0
	v_mov_b32_e32 v36, v0
	v_mov_b32_e32 v37, v0
	v_mov_b32_e32 v38, v0
	v_mov_b32_e32 v39, v0
	v_mov_b32_e32 v44, v0
	v_mov_b32_e32 v45, v0
	v_mov_b32_e32 v46, v0
	v_mov_b32_e32 v47, v0
	v_mov_b32_e32 v52, v0
	v_mov_b32_e32 v53, v0
	v_mov_b32_e32 v54, v0
	v_mov_b32_e32 v55, v0
	v_mov_b32_e32 v8, v0
	v_mov_b32_e32 v9, v0
	v_mov_b32_e32 v10, v0
	v_mov_b32_e32 v11, v0
	v_mov_b32_e32 v16, v0
	v_mov_b32_e32 v17, v0
	v_mov_b32_e32 v18, v0
	v_mov_b32_e32 v19, v0
	v_mov_b32_e32 v24, v0
	v_mov_b32_e32 v25, v0
	v_mov_b32_e32 v26, v0
	v_mov_b32_e32 v27, v0
	v_mov_b32_e32 v32, v0
	v_mov_b32_e32 v33, v0
	v_mov_b32_e32 v34, v0
	v_mov_b32_e32 v35, v0
	v_mov_b32_e32 v40, v0
	v_mov_b32_e32 v41, v0
	v_mov_b32_e32 v42, v0
	v_mov_b32_e32 v43, v0
	v_mov_b32_e32 v48, v0
	v_mov_b32_e32 v49, v0
	v_mov_b32_e32 v50, v0
	v_mov_b32_e32 v51, v0
	v_mov_b32_e32 v56, v0
	v_mov_b32_e32 v57, v0
	v_mov_b32_e32 v58, v0
	v_mov_b32_e32 v59, v0
	v_mov_b32_e32 v60, v0
	v_mov_b32_e32 v61, v0
	v_mov_b32_e32 v62, v0
	v_mov_b32_e32 v63, v0
	v_mov_b32_e32 v64, v0
	v_mov_b32_e32 v65, v0
	v_mov_b32_e32 v66, v0
	v_mov_b32_e32 v67, v0
	v_mov_b32_e32 v68, v0
	v_mov_b32_e32 v69, v0
	v_mov_b32_e32 v70, v0
	v_mov_b32_e32 v71, v0
	v_mov_b32_e32 v76, v0
	v_mov_b32_e32 v77, v0
	v_mov_b32_e32 v78, v0
	v_mov_b32_e32 v79, v0
	v_mov_b32_e32 v84, v0
	v_mov_b32_e32 v85, v0
	v_mov_b32_e32 v86, v0
	v_mov_b32_e32 v87, v0
	v_mov_b32_e32 v92, v0
	v_mov_b32_e32 v93, v0
	v_mov_b32_e32 v94, v0
	v_mov_b32_e32 v95, v0
	v_mov_b32_e32 v100, v0
	v_mov_b32_e32 v101, v0
	v_mov_b32_e32 v102, v0
	v_mov_b32_e32 v103, v0
	v_mov_b32_e32 v108, v0
	v_mov_b32_e32 v109, v0
	v_mov_b32_e32 v110, v0
	v_mov_b32_e32 v111, v0
	v_mov_b32_e32 v116, v0
	v_mov_b32_e32 v117, v0
	v_mov_b32_e32 v118, v0
	v_mov_b32_e32 v119, v0
	v_mov_b32_e32 v72, v0
	v_mov_b32_e32 v73, v0
	v_mov_b32_e32 v74, v0
	v_mov_b32_e32 v75, v0
	v_mov_b32_e32 v80, v0
	v_mov_b32_e32 v81, v0
	v_mov_b32_e32 v82, v0
	v_mov_b32_e32 v83, v0
	v_mov_b32_e32 v88, v0
	v_mov_b32_e32 v89, v0
	v_mov_b32_e32 v90, v0
	v_mov_b32_e32 v91, v0
	v_mov_b32_e32 v96, v0
	v_mov_b32_e32 v97, v0
	v_mov_b32_e32 v98, v0
	v_mov_b32_e32 v99, v0
	v_mov_b32_e32 v104, v0
	v_mov_b32_e32 v105, v0
	v_mov_b32_e32 v106, v0
	v_mov_b32_e32 v107, v0
	v_mov_b32_e32 v112, v0
	v_mov_b32_e32 v113, v0
	v_mov_b32_e32 v114, v0
	v_mov_b32_e32 v115, v0
	v_mov_b32_e32 v120, v0
	v_mov_b32_e32 v121, v0
	v_mov_b32_e32 v122, v0
	v_mov_b32_e32 v123, v0
	v_mov_b32_e32 v124, v0
	v_mov_b32_e32 v125, v0
	v_mov_b32_e32 v126, v0
	v_mov_b32_e32 v127, v0
	.p2align 6

.LBB0_339:
	s_or_b64 exec, exec, s[22:23]
	v_lshlrev_b32_e32 v46, 2, v22
	global_load_dwordx4 v[22:25], v46, s[2:3]
	global_load_dwordx4 v[26:29], v46, s[18:19]
	global_load_dwordx4 v[30:33], v46, s[2:3] offset:16
	global_load_dwordx4 v[34:37], v46, s[18:19] offset:16
	global_load_dwordx4 v[38:41], v46, s[16:17]
	global_load_dwordx4 v[42:45], v46, s[16:17] offset:16
	s_waitcnt vmcnt(0)
	v_lshlrev_b32_e32 v52, 16, v4
	v_lshlrev_b32_e32 v53, 16, v0
	v_lshlrev_b32_e32 v47, 16, v12
	v_lshlrev_b32_e32 v46, 16, v8
	v_and_b32_e32 v54, 0xffff0000, v4
	v_and_b32_e32 v55, 0xffff0000, v0
	v_and_b32_e32 v49, 0xffff0000, v12
	v_and_b32_e32 v48, 0xffff0000, v8
	v_lshlrev_b32_e32 v56, 16, v5
	v_lshlrev_b32_e32 v57, 16, v1
	v_lshlrev_b32_e32 v50, 16, v9
	v_lshlrev_b32_e32 v51, 16, v13
	v_and_b32_e32 v58, 0xffff0000, v5
	v_and_b32_e32 v59, 0xffff0000, v1
	v_and_b32_e32 v1, 0xffff0000, v13
	v_and_b32_e32 v0, 0xffff0000, v9
	v_lshlrev_b32_e32 v60, 16, v6
	v_lshlrev_b32_e32 v61, 16, v2
	v_lshlrev_b32_e32 v5, 16, v14
	v_lshlrev_b32_e32 v4, 16, v10
	v_and_b32_e32 v62, 0xffff0000, v6
	v_and_b32_e32 v63, 0xffff0000, v2
	v_and_b32_e32 v9, 0xffff0000, v14
	v_and_b32_e32 v8, 0xffff0000, v10
	v_lshlrev_b32_e32 v64, 16, v7
	v_lshlrev_b32_e32 v65, 16, v3
	v_lshlrev_b32_e32 v12, 16, v11
	v_lshlrev_b32_e32 v13, 16, v15
	v_and_b32_e32 v66, 0xffff0000, v7
	v_and_b32_e32 v67, 0xffff0000, v3
	v_and_b32_e32 v3, 0xffff0000, v15
	v_and_b32_e32 v2, 0xffff0000, v11
	v_lshlrev_b64 v[18:19], 10, v[18:19]
	v_add_u32_e32 v20, s26, v20
	v_cmp_lt_i32_e32 vcc, s29, v20
	s_or_b64 s[20:21], vcc, s[20:21]
	v_add_u32_e32 v21, s27, v21
	v_mov_b32_e32 v6, v22
	v_mov_b32_e32 v7, v26
	v_mov_b32_e32 v26, v23
	v_mov_b32_e32 v11, v28
	v_mov_b32_e32 v28, v25
	v_mov_b32_e32 v14, v30
	v_mov_b32_e32 v15, v34
	v_mov_b32_e32 v34, v31
	v_mov_b32_e32 v22, v32
	v_mov_b32_e32 v23, v36
	v_mov_b32_e32 v10, v24
	v_mov_b32_e32 v36, v33
	v_pk_mul_f32 v[6:7], v[6:7], v[46:47]
	v_pk_mul_f32 v[0:1], v[28:29], v[0:1]
	v_pk_mul_f32 v[4:5], v[14:15], v[4:5]
	v_pk_mul_f32 v[8:9], v[34:35], v[8:9]
	v_pk_mul_f32 v[12:13], v[22:23], v[12:13]
	v_pk_mul_f32 v[24:25], v[26:27], v[48:49]
	v_pk_mul_f32 v[10:11], v[10:11], v[50:51]
	v_pk_mul_f32 v[2:3], v[36:37], v[2:3]
	v_fma_f32 v6, v38, v53, v6
	v_fma_f32 v0, v41, v59, v0
	v_fma_f32 v4, v42, v61, v4
	v_fma_f32 v8, v43, v63, v8
	v_fma_f32 v12, v44, v65, v12
	v_fma_f32 v14, v39, v55, v24
	v_fma_f32 v10, v40, v57, v10
	v_fma_f32 v2, v45, v67, v2
	v_add_f32_e32 v6, v6, v7
	v_add_f32_e32 v0, v0, v1
	v_add_f32_e32 v1, v4, v5
	v_add_f32_e32 v4, v8, v9
	v_add_f32_e32 v5, v12, v13
	v_add_f32_e32 v7, v14, v25
	v_add_f32_e32 v10, v10, v11
	v_add_f32_e32 v2, v2, v3
	v_mul_f32_e32 v3, v6, v52
	v_mul_f32_e32 v4, v4, v62
	v_mul_f32_e32 v5, v5, v64
	v_mul_f32_e32 v6, v7, v54
	v_mul_f32_e32 v7, v10, v56
	v_mul_f32_e32 v8, v0, v58
	v_mul_f32_e32 v9, v1, v60
	v_mul_f32_e32 v10, v2, v66
	v_cvt_pk_bf16_f32 v0, v3, v6
	v_cvt_pk_bf16_f32 v2, v9, v4
	v_cvt_pk_bf16_f32 v3, v5, v10
	v_lshl_add_u64 v[4:5], v[18:19], 1, s[14:15]
	v_lshl_add_u64 v[4:5], v[4:5], 0, v[16:17]
	v_cvt_pk_bf16_f32 v1, v7, v8
	global_store_dwordx4 v[4:5], v[0:3], off
	s_andn2_b64 exec, exec, s[20:21]
	s_cbranch_execz .LBB0_344
	.p2align 6

.LBB0_429:
	s_add_u32 s23, s36, 0x100
	v_mov_b32_e32 v0, 0
	s_addc_u32 s25, s37, 0
	s_mov_b32 s64, -2
	s_waitcnt lgkmcnt(0)
	v_mov_b32_e32 v1, v0
	v_mov_b32_e32 v2, v0
	v_mov_b32_e32 v3, v0
	v_mov_b32_e32 v4, v0
	v_mov_b32_e32 v5, v0
	v_mov_b32_e32 v6, v0
	v_mov_b32_e32 v7, v0
	v_mov_b32_e32 v16, v0
	v_mov_b32_e32 v17, v0
	v_mov_b32_e32 v18, v0
	v_mov_b32_e32 v19, v0
	v_mov_b32_e32 v20, v0
	v_mov_b32_e32 v21, v0
	v_mov_b32_e32 v22, v0
	v_mov_b32_e32 v23, v0
	v_mov_b32_e32 v32, v0
	v_mov_b32_e32 v33, v0
	v_mov_b32_e32 v34, v0
	v_mov_b32_e32 v35, v0
	v_mov_b32_e32 v36, v0
	v_mov_b32_e32 v37, v0
	v_mov_b32_e32 v38, v0
	v_mov_b32_e32 v39, v0
	v_mov_b32_e32 v48, v0
	v_mov_b32_e32 v49, v0
	v_mov_b32_e32 v50, v0
	v_mov_b32_e32 v51, v0
	v_mov_b32_e32 v52, v0
	v_mov_b32_e32 v53, v0
	v_mov_b32_e32 v54, v0
	v_mov_b32_e32 v55, v0
	v_mov_b32_e32 v8, v0
	v_mov_b32_e32 v9, v0
	v_mov_b32_e32 v10, v0
	v_mov_b32_e32 v11, v0
	v_mov_b32_e32 v12, v0
	v_mov_b32_e32 v13, v0
	v_mov_b32_e32 v14, v0
	v_mov_b32_e32 v15, v0
	v_mov_b32_e32 v24, v0
	v_mov_b32_e32 v25, v0
	v_mov_b32_e32 v26, v0
	v_mov_b32_e32 v27, v0
	v_mov_b32_e32 v28, v0
	v_mov_b32_e32 v29, v0
	v_mov_b32_e32 v30, v0
	v_mov_b32_e32 v31, v0
	v_mov_b32_e32 v40, v0
	v_mov_b32_e32 v41, v0
	v_mov_b32_e32 v42, v0
	v_mov_b32_e32 v43, v0
	v_mov_b32_e32 v44, v0
	v_mov_b32_e32 v45, v0
	v_mov_b32_e32 v46, v0
	v_mov_b32_e32 v47, v0
	v_mov_b32_e32 v56, v0
	v_mov_b32_e32 v57, v0
	v_mov_b32_e32 v58, v0
	v_mov_b32_e32 v59, v0
	v_mov_b32_e32 v60, v0
	v_mov_b32_e32 v61, v0
	v_mov_b32_e32 v62, v0
	v_mov_b32_e32 v63, v0
	v_mov_b32_e32 v64, v0
	v_mov_b32_e32 v65, v0
	v_mov_b32_e32 v66, v0
	v_mov_b32_e32 v67, v0
	v_mov_b32_e32 v68, v0
	v_mov_b32_e32 v69, v0
	v_mov_b32_e32 v70, v0
	v_mov_b32_e32 v71, v0
	v_mov_b32_e32 v80, v0
	v_mov_b32_e32 v81, v0
	v_mov_b32_e32 v82, v0
	v_mov_b32_e32 v83, v0
	v_mov_b32_e32 v84, v0
	v_mov_b32_e32 v85, v0
	v_mov_b32_e32 v86, v0
	v_mov_b32_e32 v87, v0
	v_mov_b32_e32 v96, v0
	v_mov_b32_e32 v97, v0
	v_mov_b32_e32 v98, v0
	v_mov_b32_e32 v99, v0
	v_mov_b32_e32 v100, v0
	v_mov_b32_e32 v101, v0
	v_mov_b32_e32 v102, v0
	v_mov_b32_e32 v103, v0
	v_mov_b32_e32 v120, v0
	v_mov_b32_e32 v121, v0
	v_mov_b32_e32 v122, v0
	v_mov_b32_e32 v123, v0
	v_mov_b32_e32 v132, v0
	v_mov_b32_e32 v133, v0
	v_mov_b32_e32 v134, v0
	v_mov_b32_e32 v135, v0
	v_mov_b32_e32 v72, v0
	v_mov_b32_e32 v73, v0
	v_mov_b32_e32 v74, v0
	v_mov_b32_e32 v75, v0
	v_mov_b32_e32 v76, v0
	v_mov_b32_e32 v77, v0
	v_mov_b32_e32 v78, v0
	v_mov_b32_e32 v79, v0
	v_mov_b32_e32 v88, v0
	v_mov_b32_e32 v89, v0
	v_mov_b32_e32 v90, v0
	v_mov_b32_e32 v91, v0
	v_mov_b32_e32 v92, v0
	v_mov_b32_e32 v93, v0
	v_mov_b32_e32 v94, v0
	v_mov_b32_e32 v95, v0
	v_mov_b32_e32 v104, v0
	v_mov_b32_e32 v105, v0
	v_mov_b32_e32 v106, v0
	v_mov_b32_e32 v107, v0
	v_mov_b32_e32 v108, v0
	v_mov_b32_e32 v109, v0
	v_mov_b32_e32 v110, v0
	v_mov_b32_e32 v111, v0
	v_mov_b32_e32 v144, v0
	v_mov_b32_e32 v145, v0
	s_waitcnt vmcnt(0)
	v_mov_b32_e32 v146, v0
	v_mov_b32_e32 v147, v0
	v_mov_b32_e32 v152, v0
	v_mov_b32_e32 v153, v0
	v_mov_b32_e32 v154, v0
	v_mov_b32_e32 v155, v0
	.p2align 6

.LBB0_544:
	s_add_u32 s21, s36, 0x100
	s_addc_u32 s66, s37, 0
	v_lshl_add_u64 v[76:77], s[22:23], 0, v[68:69]
	v_lshl_add_u64 v[78:79], s[22:23], 0, v[70:71]
	s_mov_b32 s67, -2
	s_mov_b64 s[36:37], 0
	.p2align 6

.LBB0_642:
	ds_read2_b32 v[214:215], v146 offset1:32
	s_addk_i32 s24, 0x400
	s_addk_i32 s52, 0x400
	s_add_i32 s53, s53, 0x10000
	s_waitcnt vmcnt(0) lgkmcnt(0)
	v_mul_f32_e32 v77, v68, v214
	ds_read_b32 v209, v147
	ds_read_b32 v211, v148
	ds_read_b32 v212, v149
	ds_read_b32 v213, v150
	ds_read_b32 v214, v151
	ds_read_b32 v216, v152
	ds_read_b32 v217, v153
	ds_read_b32 v218, v154
	s_waitcnt lgkmcnt(7)
	v_mul_f32_e32 v209, v69, v209
	v_cvt_pk_bf16_f32 v210, v77, v209
	s_waitcnt lgkmcnt(6)
	v_mul_f32_e32 v77, v70, v211
	s_waitcnt lgkmcnt(5)
	v_mul_f32_e32 v209, v71, v212
	v_cvt_pk_bf16_f32 v211, v77, v209
	s_waitcnt lgkmcnt(4)
	v_mul_f32_e32 v77, v64, v213
	s_waitcnt lgkmcnt(3)
	v_mul_f32_e32 v209, v65, v214
	v_cvt_pk_bf16_f32 v212, v77, v209
	s_waitcnt lgkmcnt(2)
	v_mul_f32_e32 v77, v66, v216
	s_waitcnt lgkmcnt(1)
	v_mul_f32_e32 v209, v67, v217
	v_cvt_pk_bf16_f32 v213, v77, v209
	v_add_u32_e32 v77, s26, v138
	v_mad_i64_i32 v[216:217], s[4:5], s25, v77, 0
	v_lshl_add_u64 v[216:217], v[216:217], 1, s[2:3]
	s_lshl_b64 s[4:5], s[6:7], 1
	v_lshl_add_u64 v[216:217], v[216:217], 0, s[4:5]
	v_lshl_add_u64 v[216:217], v[216:217], 0, v[72:73]
	global_store_dwordx4 v[216:217], v[210:213], off
	s_waitcnt lgkmcnt(0)
	v_mul_f32_e32 v77, v68, v218
	ds_read_b32 v209, v155
	ds_read_b32 v211, v156
	ds_read_b32 v212, v157
	ds_read_b32 v213, v158
	ds_read_b32 v214, v159
	ds_read_b32 v216, v160
	ds_read_b32 v217, v161
	ds_read_b32 v218, v162
	s_waitcnt lgkmcnt(7)
	v_mul_f32_e32 v209, v69, v209
	v_cvt_pk_bf16_f32 v210, v77, v209
	s_waitcnt lgkmcnt(6)
	v_mul_f32_e32 v77, v70, v211
	s_waitcnt lgkmcnt(5)
	v_mul_f32_e32 v209, v71, v212
	v_cvt_pk_bf16_f32 v211, v77, v209
	s_waitcnt lgkmcnt(4)
	v_mul_f32_e32 v77, v64, v213
	s_waitcnt lgkmcnt(3)
	v_mul_f32_e32 v209, v65, v214
	v_cvt_pk_bf16_f32 v212, v77, v209
	s_waitcnt lgkmcnt(2)
	v_mul_f32_e32 v77, v66, v216
	s_waitcnt lgkmcnt(1)
	v_mul_f32_e32 v209, v67, v217
	v_cvt_pk_bf16_f32 v213, v77, v209
	v_add_u32_e32 v77, s26, v139
	v_mad_i64_i32 v[216:217], s[6:7], s25, v77, 0
	v_lshl_add_u64 v[216:217], v[216:217], 1, s[2:3]
	v_lshl_add_u64 v[216:217], v[216:217], 0, s[4:5]
	v_lshl_add_u64 v[216:217], v[216:217], 0, v[72:73]
	global_store_dwordx4 v[216:217], v[210:213], off
	s_waitcnt lgkmcnt(0)
	v_mul_f32_e32 v77, v68, v218
	ds_read_b32 v209, v163
	ds_read_b32 v211, v164
	ds_read_b32 v212, v165
	ds_read_b32 v213, v166
	ds_read_b32 v214, v167
	ds_read_b32 v216, v168
	ds_read_b32 v217, v169
	ds_read_b32 v218, v170
	s_waitcnt lgkmcnt(7)
	v_mul_f32_e32 v209, v69, v209
	v_cvt_pk_bf16_f32 v210, v77, v209
	s_waitcnt lgkmcnt(6)
	v_mul_f32_e32 v77, v70, v211
	s_waitcnt lgkmcnt(5)
	v_mul_f32_e32 v209, v71, v212
	v_cvt_pk_bf16_f32 v211, v77, v209
	s_waitcnt lgkmcnt(4)
	v_mul_f32_e32 v77, v64, v213
	s_waitcnt lgkmcnt(3)
	v_mul_f32_e32 v209, v65, v214
	v_cvt_pk_bf16_f32 v212, v77, v209
	s_waitcnt lgkmcnt(2)
	v_mul_f32_e32 v77, v66, v216
	s_waitcnt lgkmcnt(1)
	v_mul_f32_e32 v209, v67, v217
	v_cvt_pk_bf16_f32 v213, v77, v209
	v_add_u32_e32 v77, s26, v140
	v_mad_i64_i32 v[216:217], s[6:7], s25, v77, 0
	v_lshl_add_u64 v[216:217], v[216:217], 1, s[2:3]
	v_lshl_add_u64 v[216:217], v[216:217], 0, s[4:5]
	v_lshl_add_u64 v[216:217], v[216:217], 0, v[72:73]
	global_store_dwordx4 v[216:217], v[210:213], off
	s_waitcnt lgkmcnt(0)
	v_mul_f32_e32 v77, v68, v218
	ds_read_b32 v209, v171
	ds_read_b32 v211, v172
	ds_read_b32 v212, v173
	ds_read_b32 v213, v174
	ds_read_b32 v214, v175
	ds_read_b32 v216, v176
	ds_read_b32 v217, v177
	ds_read_b32 v218, v178
	s_waitcnt lgkmcnt(7)
	v_mul_f32_e32 v209, v69, v209
	v_cvt_pk_bf16_f32 v210, v77, v209
	s_waitcnt lgkmcnt(6)
	v_mul_f32_e32 v77, v70, v211
	s_waitcnt lgkmcnt(5)
	v_mul_f32_e32 v209, v71, v212
	v_cvt_pk_bf16_f32 v211, v77, v209
	s_waitcnt lgkmcnt(4)
	v_mul_f32_e32 v77, v64, v213
	s_waitcnt lgkmcnt(3)
	v_mul_f32_e32 v209, v65, v214
	v_cvt_pk_bf16_f32 v212, v77, v209
	s_waitcnt lgkmcnt(2)
	v_mul_f32_e32 v77, v66, v216
	s_waitcnt lgkmcnt(1)
	v_mul_f32_e32 v209, v67, v217
	v_cvt_pk_bf16_f32 v213, v77, v209
	v_add_u32_e32 v77, s26, v141
	v_mad_i64_i32 v[216:217], s[6:7], s25, v77, 0
	v_lshl_add_u64 v[216:217], v[216:217], 1, s[2:3]
	v_lshl_add_u64 v[216:217], v[216:217], 0, s[4:5]
	v_lshl_add_u64 v[216:217], v[216:217], 0, v[72:73]
	global_store_dwordx4 v[216:217], v[210:213], off
	v_mul_f32_e32 v77, v68, v215
	s_waitcnt lgkmcnt(0)
	v_mul_f32_e32 v209, v69, v218
	v_cvt_pk_bf16_f32 v210, v77, v209
	ds_read_b32 v77, v179
	ds_read_b32 v209, v180
	ds_read_b32 v212, v181
	ds_read_b32 v213, v182
	ds_read_b32 v214, v183
	ds_read_b32 v215, v184
	ds_read_b32 v216, v185
	ds_read_b32 v217, v186
	s_waitcnt lgkmcnt(7)
	v_mul_f32_e32 v77, v70, v77
	s_waitcnt lgkmcnt(6)
	v_mul_f32_e32 v209, v71, v209
	v_cvt_pk_bf16_f32 v211, v77, v209
	s_waitcnt lgkmcnt(5)
	v_mul_f32_e32 v77, v64, v212
	s_waitcnt lgkmcnt(4)
	v_mul_f32_e32 v209, v65, v213
	v_cvt_pk_bf16_f32 v212, v77, v209
	s_waitcnt lgkmcnt(3)
	v_mul_f32_e32 v77, v66, v214
	s_waitcnt lgkmcnt(2)
	v_mul_f32_e32 v209, v67, v215
	v_cvt_pk_bf16_f32 v213, v77, v209
	v_add_u32_e32 v77, s26, v142
	v_mad_i64_i32 v[214:215], s[6:7], s25, v77, 0
	v_lshl_add_u64 v[214:215], v[214:215], 1, s[2:3]
	v_lshl_add_u64 v[214:215], v[214:215], 0, s[4:5]
	v_lshl_add_u64 v[214:215], v[214:215], 0, v[72:73]
	global_store_dwordx4 v[214:215], v[210:213], off
	s_waitcnt lgkmcnt(1)
	v_mul_f32_e32 v77, v68, v216
	s_waitcnt lgkmcnt(0)
	v_mul_f32_e32 v209, v69, v217
	v_cvt_pk_bf16_f32 v210, v77, v209
	ds_read_b32 v77, v187
	ds_read_b32 v209, v188
	ds_read_b32 v212, v189
	ds_read_b32 v213, v190
	ds_read_b32 v214, v191
	ds_read_b32 v215, v192
	ds_read_b32 v216, v193
	ds_read_b32 v217, v194
	s_waitcnt lgkmcnt(7)
	v_mul_f32_e32 v77, v70, v77
	s_waitcnt lgkmcnt(6)
	v_mul_f32_e32 v209, v71, v209
	v_cvt_pk_bf16_f32 v211, v77, v209
	s_waitcnt lgkmcnt(5)
	v_mul_f32_e32 v77, v64, v212
	s_waitcnt lgkmcnt(4)
	v_mul_f32_e32 v209, v65, v213
	v_cvt_pk_bf16_f32 v212, v77, v209
	s_waitcnt lgkmcnt(3)
	v_mul_f32_e32 v77, v66, v214
	s_waitcnt lgkmcnt(2)
	v_mul_f32_e32 v209, v67, v215
	v_cvt_pk_bf16_f32 v213, v77, v209
	v_add_u32_e32 v77, s26, v143
	v_mad_i64_i32 v[214:215], s[6:7], s25, v77, 0
	v_lshl_add_u64 v[214:215], v[214:215], 1, s[2:3]
	v_lshl_add_u64 v[214:215], v[214:215], 0, s[4:5]
	v_lshl_add_u64 v[214:215], v[214:215], 0, v[72:73]
	global_store_dwordx4 v[214:215], v[210:213], off
	s_waitcnt lgkmcnt(1)
	v_mul_f32_e32 v77, v68, v216
	s_waitcnt lgkmcnt(0)
	v_mul_f32_e32 v209, v69, v217
	v_cvt_pk_bf16_f32 v210, v77, v209
	ds_read_b32 v77, v195
	ds_read_b32 v209, v196
	ds_read_b32 v212, v197
	ds_read_b32 v213, v198
	ds_read_b32 v214, v199
	ds_read_b32 v215, v200
	ds_read_b32 v216, v201
	ds_read_b32 v217, v202
	s_waitcnt lgkmcnt(7)
	v_mul_f32_e32 v77, v70, v77
	s_waitcnt lgkmcnt(6)
	v_mul_f32_e32 v209, v71, v209
	v_cvt_pk_bf16_f32 v211, v77, v209
	s_waitcnt lgkmcnt(5)
	v_mul_f32_e32 v77, v64, v212
	s_waitcnt lgkmcnt(4)
	v_mul_f32_e32 v209, v65, v213
	v_cvt_pk_bf16_f32 v212, v77, v209
	s_waitcnt lgkmcnt(3)
	v_mul_f32_e32 v77, v66, v214
	s_waitcnt lgkmcnt(2)
	v_mul_f32_e32 v209, v67, v215
	v_cvt_pk_bf16_f32 v213, v77, v209
	v_add_u32_e32 v77, s26, v144
	v_mad_i64_i32 v[214:215], s[6:7], s25, v77, 0
	v_lshl_add_u64 v[214:215], v[214:215], 1, s[2:3]
	v_lshl_add_u64 v[214:215], v[214:215], 0, s[4:5]
	v_lshl_add_u64 v[214:215], v[214:215], 0, v[72:73]
	global_store_dwordx4 v[214:215], v[210:213], off
	ds_read_b32 v77, v203
	ds_read_b32 v209, v204
	ds_read_b32 v210, v205
	ds_read_b32 v211, v206
	ds_read_b32 v212, v207
	ds_read_b32 v213, v208
	s_waitcnt lgkmcnt(7)
	v_mul_f32_e32 v68, v68, v216
	s_waitcnt lgkmcnt(6)
	v_mul_f32_e32 v69, v69, v217
	v_cvt_pk_bf16_f32 v68, v68, v69
	s_waitcnt lgkmcnt(5)
	v_mul_f32_e32 v69, v70, v77
	s_waitcnt lgkmcnt(4)
	v_mul_f32_e32 v70, v71, v209
	s_waitcnt lgkmcnt(3)
	v_mul_f32_e32 v64, v64, v210
	v_cvt_pk_bf16_f32 v69, v69, v70
	s_waitcnt lgkmcnt(2)
	v_mul_f32_e32 v65, v65, v211
	v_cvt_pk_bf16_f32 v70, v64, v65
	s_waitcnt lgkmcnt(1)
	v_mul_f32_e32 v64, v66, v212
	s_waitcnt lgkmcnt(0)
	v_mul_f32_e32 v65, v67, v213
	v_cvt_pk_bf16_f32 v71, v64, v65
	v_add_u32_e32 v64, s26, v145
	v_mad_i64_i32 v[64:65], s[6:7], s25, v64, 0
	v_lshl_add_u64 v[64:65], v[64:65], 1, s[2:3]
	v_lshl_add_u64 v[64:65], v[64:65], 0, s[4:5]
	v_lshl_add_u64 v[64:65], v[64:65], 0, v[72:73]
	global_store_dwordx4 v[64:65], v[68:71], off
	s_waitcnt lgkmcnt(0)
	s_cmpk_lt_i32 s54, 0x400
	s_mov_b32 s26, s22
	s_mov_b64 s[2:3], s[8:9]
	s_mov_b64 s[4:5], s[12:13]
	s_mov_b32 s25, s55
	s_mov_b32 s6, s16
	s_cbranch_scc0 .LBB0_676
	.p2align 6

.LBB0_742:
	s_cmp_gt_i32 s34, 11
	s_cselect_b64 s[2:3], -1, 0
	s_cmp_lt_i32 s35, 12
	s_cselect_b64 s[4:5], -1, 0
	s_or_b64 s[2:3], s[2:3], s[4:5]
	s_and_b64 vcc, exec, s[2:3]
	s_cbranch_vccnz .LBB0_1038
	s_mov_b32 s2, 24
	s_lshl_b32 s2, s2, 3
	s_add_i32 s2, s2, 0
	s_add_i32 s2, s2, 0x201c0
	v_mov_b32_e32 v0, s2
	s_waitcnt vmcnt(0) lgkmcnt(0)
	ds_read_b32 v1, v0
	ds_read_b32 v0, v0 offset:4
	s_and_b32 s42, s33, 0xffffffc0
	v_mbcnt_lo_u32_b32 v2, -1, 0
	v_mbcnt_hi_u32_b32 v2, -1, v2
	s_waitcnt lgkmcnt(1)
	v_readfirstlane_b32 s2, v1
	s_waitcnt lgkmcnt(0)
	v_readfirstlane_b32 s3, v0
	v_add_u32_e32 v0, s42, v2
	v_cmp_gt_i32_e32 vcc, 64, v0
	s_and_saveexec_b64 s[4:5], vcc
	s_cbranch_execz .LBB0_759
	v_lshlrev_b32_e32 v2, 5, v0
	v_ashrrev_i32_e32 v3, 31, v2
	v_lshl_add_u64 v[2:3], v[2:3], 2, s[2:3]
	v_add_co_u32_e32 v2, vcc, 0x8000, v2
	v_lshlrev_b32_e32 v9, 2, v0
	s_nop 0
	v_addc_co_u32_e32 v3, vcc, 0, v3, vcc
	global_load_dword v8, v[2:3], off sc1
	v_add_u32_e32 v1, -4, v9
	v_cmp_lt_i32_e32 vcc, 0, v0
	v_add_u32_e32 v4, -8, v9
	v_add_u32_e32 v5, -16, v9
	v_subrev_u32_e32 v6, 32, v9
	v_subrev_u32_e32 v7, 64, v9
	v_add_u32_e32 v10, 0xffffff80, v9
	v_add_u32_e32 v9, 0, v9
	v_add_u32_e32 v9, 0x20a00, v9
	s_waitcnt vmcnt(0)
	v_add_u32_e32 v2, 0xff, v8
	v_ashrrev_i32_e32 v2, 8, v2
	ds_bpermute_b32 v1, v1, v2
	ds_write_b32 v9, v8
	s_waitcnt lgkmcnt(1)
	v_cndmask_b32_e32 v3, 0, v1, vcc
	v_add_u32_e32 v1, v3, v2
	ds_bpermute_b32 v4, v4, v1
	v_cmp_lt_i32_e32 vcc, 1, v0
	s_waitcnt lgkmcnt(0)
	s_nop 0
	v_cndmask_b32_e32 v4, 0, v4, vcc
	v_add_u32_e32 v1, v4, v1
	ds_bpermute_b32 v5, v5, v1
	v_cmp_lt_i32_e32 vcc, 3, v0
	s_waitcnt lgkmcnt(0)
	s_nop 0
	v_cndmask_b32_e32 v5, 0, v5, vcc
	v_add_u32_e32 v1, v5, v1
	ds_bpermute_b32 v6, v6, v1
	v_cmp_lt_i32_e32 vcc, 7, v0
	s_waitcnt lgkmcnt(0)
	s_nop 0
	v_cndmask_b32_e32 v6, 0, v6, vcc
	v_add_u32_e32 v1, v6, v1
	ds_bpermute_b32 v7, v7, v1
	v_cmp_lt_i32_e32 vcc, 15, v0
	s_waitcnt lgkmcnt(0)
	s_nop 0
	v_cndmask_b32_e32 v7, 0, v7, vcc
	v_add_u32_e32 v1, v7, v1
	ds_bpermute_b32 v10, v10, v1
	v_cmp_lt_i32_e32 vcc, 31, v0
	s_waitcnt lgkmcnt(0)
	s_nop 0
	v_cndmask_b32_e32 v9, 0, v10, vcc
	v_cmp_eq_u32_e32 vcc, 63, v0
	s_and_saveexec_b64 s[6:7], vcc
	s_add_i32 s8, 0, 0x20b00
	v_add_u32_e32 v1, v9, v1
	v_mov_b32_e32 v8, s8
	ds_write_b32 v8, v1
	s_or_b64 exec, exec, s[6:7]
	v_cmp_lt_i32_e32 vcc, 0, v2
	s_and_b64 exec, exec, vcc
	s_cbranch_execz .LBB0_759
	v_lshlrev_b32_e32 v8, 16, v0
	v_cmp_ne_u32_e32 vcc, 1, v2
	s_mov_b64 s[8:9], -1
	v_mov_b32_e32 v0, 0
	s_and_saveexec_b64 s[6:7], vcc
	s_cbranch_execz .LBB0_756
	v_add_u32_e32 v0, -2, v2
	v_lshrrev_b32_e32 v1, 1, v0
	v_cmp_lt_u32_e32 vcc, 13, v0
	v_mov_b32_e32 v0, 0
	v_add_u32_e32 v10, 1, v1
	s_mov_b32 s16, 0
	v_mov_b32_e32 v1, 1
	v_mov_b32_e32 v13, v0
	s_and_saveexec_b64 s[8:9], vcc
	s_cbranch_execz .LBB0_752
	v_add_u32_e32 v0, v3, v4
	v_add3_u32 v0, v0, v5, v6
	v_add3_u32 v0, v0, v7, v9
	v_lshl_add_u32 v0, v0, 2, 0
	v_and_b32_e32 v11, -8, v10
	v_add_u32_e32 v12, 0x20400, v0
	s_mov_b32 s15, 1
	s_mov_b64 s[12:13], 0
	s_mov_b32 s14, 0
	.p2align 6

.LBB0_752:
	s_or_b64 exec, exec, s[8:9]
	v_and_b32_e32 v10, 7, v10
	v_cmp_ne_u32_e32 vcc, 0, v10
	s_and_saveexec_b64 s[8:9], vcc
	s_cbranch_execz .LBB0_755
	v_add3_u32 v12, v3, v4, v5
	v_add3_u32 v12, v12, v6, v7
	v_lshlrev_b32_e32 v11, 2, v13
	v_add_lshl_u32 v12, v12, v9, 2
	v_add3_u32 v11, v11, v12, 0
	v_add_u32_e32 v11, 0x20400, v11
	s_mov_b64 s[12:13], 0
	.p2align 6

.LBB0_756:
	s_or_b64 exec, exec, s[6:7]
	s_and_b64 exec, exec, s[8:9]
	s_cbranch_execz .LBB0_759
	v_add3_u32 v3, v3, v4, v5
	v_add3_u32 v3, v3, v6, v7
	v_lshlrev_b32_e32 v1, 2, v0
	v_add_lshl_u32 v3, v3, v9, 2
	v_add3_u32 v1, v1, v3, 0
	v_add_u32_e32 v1, 0x20400, v1
	s_mov_b64 s[6:7], 0
	.p2align 6

.LBB0_790:
	s_add_u32 s23, s36, 0x100
	s_addc_u32 s66, s37, 0
	s_add_u32 s36, s30, 0x80
	v_mov_b32_e32 v135, v133
	v_mov_b32_e32 v141, v133
	s_addc_u32 s37, s31, 0
	v_mov_b32_e32 v0, 0
	v_lshl_add_u64 v[142:143], s[36:37], 0, v[140:141]
	v_lshl_add_u64 v[144:145], s[36:37], 0, v[134:135]
	s_mov_b32 s67, -2
	s_mov_b64 s[36:37], 0
	v_mov_b32_e32 v1, v0
	v_mov_b32_e32 v2, v0
	v_mov_b32_e32 v3, v0
	v_mov_b32_e32 v4, v0
	v_mov_b32_e32 v5, v0
	v_mov_b32_e32 v6, v0
	v_mov_b32_e32 v7, v0
	v_mov_b32_e32 v16, v0
	v_mov_b32_e32 v17, v0
	v_mov_b32_e32 v18, v0
	v_mov_b32_e32 v19, v0
	v_mov_b32_e32 v20, v0
	v_mov_b32_e32 v21, v0
	v_mov_b32_e32 v22, v0
	v_mov_b32_e32 v23, v0
	v_mov_b32_e32 v32, v0
	v_mov_b32_e32 v33, v0
	v_mov_b32_e32 v34, v0
	v_mov_b32_e32 v35, v0
	v_mov_b32_e32 v36, v0
	v_mov_b32_e32 v37, v0
	v_mov_b32_e32 v38, v0
	v_mov_b32_e32 v39, v0
	v_mov_b32_e32 v48, v0
	v_mov_b32_e32 v49, v0
	v_mov_b32_e32 v50, v0
	v_mov_b32_e32 v51, v0
	v_mov_b32_e32 v52, v0
	v_mov_b32_e32 v53, v0
	v_mov_b32_e32 v54, v0
	v_mov_b32_e32 v55, v0
	v_mov_b32_e32 v8, v0
	v_mov_b32_e32 v9, v0
	v_mov_b32_e32 v10, v0
	v_mov_b32_e32 v11, v0
	v_mov_b32_e32 v12, v0
	v_mov_b32_e32 v13, v0
	v_mov_b32_e32 v14, v0
	v_mov_b32_e32 v15, v0
	v_mov_b32_e32 v24, v0
	v_mov_b32_e32 v25, v0
	v_mov_b32_e32 v26, v0
	v_mov_b32_e32 v27, v0
	v_mov_b32_e32 v28, v0
	v_mov_b32_e32 v29, v0
	v_mov_b32_e32 v30, v0
	v_mov_b32_e32 v31, v0
	v_mov_b32_e32 v40, v0
	v_mov_b32_e32 v41, v0
	v_mov_b32_e32 v42, v0
	v_mov_b32_e32 v43, v0
	v_mov_b32_e32 v44, v0
	v_mov_b32_e32 v45, v0
	v_mov_b32_e32 v46, v0
	v_mov_b32_e32 v47, v0
	v_mov_b32_e32 v56, v0
	v_mov_b32_e32 v57, v0
	v_mov_b32_e32 v58, v0
	v_mov_b32_e32 v59, v0
	v_mov_b32_e32 v60, v0
	v_mov_b32_e32 v61, v0
	v_mov_b32_e32 v62, v0
	v_mov_b32_e32 v63, v0
	v_mov_b32_e32 v64, v0
	v_mov_b32_e32 v65, v0
	v_mov_b32_e32 v66, v0
	v_mov_b32_e32 v67, v0
	v_mov_b32_e32 v68, v0
	v_mov_b32_e32 v69, v0
	v_mov_b32_e32 v70, v0
	v_mov_b32_e32 v71, v0
	v_mov_b32_e32 v80, v0
	v_mov_b32_e32 v81, v0
	v_mov_b32_e32 v82, v0
	v_mov_b32_e32 v83, v0
	v_mov_b32_e32 v84, v0
	v_mov_b32_e32 v85, v0
	v_mov_b32_e32 v86, v0
	v_mov_b32_e32 v87, v0
	v_mov_b32_e32 v96, v0
	v_mov_b32_e32 v97, v0
	v_mov_b32_e32 v98, v0
	v_mov_b32_e32 v99, v0
	v_mov_b32_e32 v100, v0
	v_mov_b32_e32 v101, v0
	v_mov_b32_e32 v102, v0
	v_mov_b32_e32 v103, v0
	v_mov_b32_e32 v120, v0
	v_mov_b32_e32 v121, v0
	v_mov_b32_e32 v122, v0
	v_mov_b32_e32 v123, v0
	v_mov_b32_e32 v124, v0
	v_mov_b32_e32 v125, v0
	v_mov_b32_e32 v126, v0
	v_mov_b32_e32 v127, v0
	v_mov_b32_e32 v72, v0
	v_mov_b32_e32 v73, v0
	v_mov_b32_e32 v74, v0
	v_mov_b32_e32 v75, v0
	v_mov_b32_e32 v76, v0
	v_mov_b32_e32 v77, v0
	v_mov_b32_e32 v78, v0
	v_mov_b32_e32 v79, v0
	v_mov_b32_e32 v88, v0
	v_mov_b32_e32 v89, v0
	v_mov_b32_e32 v90, v0
	v_mov_b32_e32 v91, v0
	v_mov_b32_e32 v92, v0
	v_mov_b32_e32 v93, v0
	v_mov_b32_e32 v94, v0
	v_mov_b32_e32 v95, v0
	v_mov_b32_e32 v104, v0
	v_mov_b32_e32 v105, v0
	v_mov_b32_e32 v106, v0
	v_mov_b32_e32 v107, v0
	v_mov_b32_e32 v108, v0
	v_mov_b32_e32 v109, v0
	v_mov_b32_e32 v110, v0
	v_mov_b32_e32 v111, v0
	v_mov_b32_e32 v112, v0
	v_mov_b32_e32 v113, v0
	v_mov_b32_e32 v114, v0
	v_mov_b32_e32 v115, v0
	v_mov_b32_e32 v116, v0
	v_mov_b32_e32 v117, v0
	v_mov_b32_e32 v118, v0
	v_mov_b32_e32 v119, v0
	.p2align 6

.LBB0_851:
	ds_read2_b32 v[214:215], v146 offset1:32
	s_addk_i32 s30, 0x800
	s_addk_i32 s56, 0x800
	s_add_i32 s57, s57, 0x20000
	s_andn2_b64 vcc, exec, s[12:13]
	s_waitcnt vmcnt(0) lgkmcnt(0)
	v_mul_f32_e32 v77, v68, v214
	ds_read_b32 v209, v147
	ds_read_b32 v211, v148
	ds_read_b32 v212, v149
	ds_read_b32 v213, v150
	ds_read_b32 v214, v151
	ds_read_b32 v216, v152
	ds_read_b32 v217, v153
	ds_read_b32 v218, v154
	s_waitcnt lgkmcnt(7)
	v_mul_f32_e32 v209, v69, v209
	v_cvt_pk_bf16_f32 v210, v77, v209
	s_waitcnt lgkmcnt(6)
	v_mul_f32_e32 v77, v70, v211
	s_waitcnt lgkmcnt(5)
	v_mul_f32_e32 v209, v71, v212
	v_cvt_pk_bf16_f32 v211, v77, v209
	s_waitcnt lgkmcnt(4)
	v_mul_f32_e32 v77, v64, v213
	s_waitcnt lgkmcnt(3)
	v_mul_f32_e32 v209, v65, v214
	v_cvt_pk_bf16_f32 v212, v77, v209
	s_waitcnt lgkmcnt(2)
	v_mul_f32_e32 v77, v66, v216
	s_waitcnt lgkmcnt(1)
	v_mul_f32_e32 v209, v67, v217
	v_cvt_pk_bf16_f32 v213, v77, v209
	v_add_u32_e32 v77, s36, v138
	v_mad_i64_i32 v[216:217], s[6:7], s31, v77, 0
	v_lshl_add_u64 v[216:217], v[216:217], 1, s[2:3]
	s_lshl_b64 s[6:7], s[8:9], 1
	v_lshl_add_u64 v[216:217], v[216:217], 0, s[6:7]
	v_lshl_add_u64 v[216:217], v[216:217], 0, v[72:73]
	global_store_dwordx4 v[216:217], v[210:213], off
	s_waitcnt lgkmcnt(0)
	v_mul_f32_e32 v77, v68, v218
	ds_read_b32 v209, v155
	ds_read_b32 v211, v156
	ds_read_b32 v212, v157
	ds_read_b32 v213, v158
	ds_read_b32 v214, v159
	ds_read_b32 v216, v160
	ds_read_b32 v217, v161
	ds_read_b32 v218, v162
	s_waitcnt lgkmcnt(7)
	v_mul_f32_e32 v209, v69, v209
	v_cvt_pk_bf16_f32 v210, v77, v209
	s_waitcnt lgkmcnt(6)
	v_mul_f32_e32 v77, v70, v211
	s_waitcnt lgkmcnt(5)
	v_mul_f32_e32 v209, v71, v212
	v_cvt_pk_bf16_f32 v211, v77, v209
	s_waitcnt lgkmcnt(4)
	v_mul_f32_e32 v77, v64, v213
	s_waitcnt lgkmcnt(3)
	v_mul_f32_e32 v209, v65, v214
	v_cvt_pk_bf16_f32 v212, v77, v209
	s_waitcnt lgkmcnt(2)
	v_mul_f32_e32 v77, v66, v216
	s_waitcnt lgkmcnt(1)
	v_mul_f32_e32 v209, v67, v217
	v_cvt_pk_bf16_f32 v213, v77, v209
	v_add_u32_e32 v77, s36, v139
	v_mad_i64_i32 v[216:217], s[8:9], s31, v77, 0
	v_lshl_add_u64 v[216:217], v[216:217], 1, s[2:3]
	v_lshl_add_u64 v[216:217], v[216:217], 0, s[6:7]
	v_lshl_add_u64 v[216:217], v[216:217], 0, v[72:73]
	global_store_dwordx4 v[216:217], v[210:213], off
	s_waitcnt lgkmcnt(0)
	v_mul_f32_e32 v77, v68, v218
	ds_read_b32 v209, v163
	ds_read_b32 v211, v164
	ds_read_b32 v212, v165
	ds_read_b32 v213, v166
	ds_read_b32 v214, v167
	ds_read_b32 v216, v168
	ds_read_b32 v217, v169
	ds_read_b32 v218, v170
	s_waitcnt lgkmcnt(7)
	v_mul_f32_e32 v209, v69, v209
	v_cvt_pk_bf16_f32 v210, v77, v209
	s_waitcnt lgkmcnt(6)
	v_mul_f32_e32 v77, v70, v211
	s_waitcnt lgkmcnt(5)
	v_mul_f32_e32 v209, v71, v212
	v_cvt_pk_bf16_f32 v211, v77, v209
	s_waitcnt lgkmcnt(4)
	v_mul_f32_e32 v77, v64, v213
	s_waitcnt lgkmcnt(3)
	v_mul_f32_e32 v209, v65, v214
	v_cvt_pk_bf16_f32 v212, v77, v209
	s_waitcnt lgkmcnt(2)
	v_mul_f32_e32 v77, v66, v216
	s_waitcnt lgkmcnt(1)
	v_mul_f32_e32 v209, v67, v217
	v_cvt_pk_bf16_f32 v213, v77, v209
	v_add_u32_e32 v77, s36, v140
	v_mad_i64_i32 v[216:217], s[8:9], s31, v77, 0
	v_lshl_add_u64 v[216:217], v[216:217], 1, s[2:3]
	v_lshl_add_u64 v[216:217], v[216:217], 0, s[6:7]
	v_lshl_add_u64 v[216:217], v[216:217], 0, v[72:73]
	global_store_dwordx4 v[216:217], v[210:213], off
	s_waitcnt lgkmcnt(0)
	v_mul_f32_e32 v77, v68, v218
	ds_read_b32 v209, v171
	ds_read_b32 v211, v172
	ds_read_b32 v212, v173
	ds_read_b32 v213, v174
	ds_read_b32 v214, v175
	ds_read_b32 v216, v176
	ds_read_b32 v217, v177
	ds_read_b32 v218, v178
	s_waitcnt lgkmcnt(7)
	v_mul_f32_e32 v209, v69, v209
	v_cvt_pk_bf16_f32 v210, v77, v209
	s_waitcnt lgkmcnt(6)
	v_mul_f32_e32 v77, v70, v211
	s_waitcnt lgkmcnt(5)
	v_mul_f32_e32 v209, v71, v212
	v_cvt_pk_bf16_f32 v211, v77, v209
	s_waitcnt lgkmcnt(4)
	v_mul_f32_e32 v77, v64, v213
	s_waitcnt lgkmcnt(3)
	v_mul_f32_e32 v209, v65, v214
	v_cvt_pk_bf16_f32 v212, v77, v209
	s_waitcnt lgkmcnt(2)
	v_mul_f32_e32 v77, v66, v216
	s_waitcnt lgkmcnt(1)
	v_mul_f32_e32 v209, v67, v217
	v_cvt_pk_bf16_f32 v213, v77, v209
	v_add_u32_e32 v77, s36, v141
	v_mad_i64_i32 v[216:217], s[8:9], s31, v77, 0
	v_lshl_add_u64 v[216:217], v[216:217], 1, s[2:3]
	v_lshl_add_u64 v[216:217], v[216:217], 0, s[6:7]
	v_lshl_add_u64 v[216:217], v[216:217], 0, v[72:73]
	global_store_dwordx4 v[216:217], v[210:213], off
	v_mul_f32_e32 v77, v68, v215
	s_waitcnt lgkmcnt(0)
	v_mul_f32_e32 v209, v69, v218
	v_cvt_pk_bf16_f32 v210, v77, v209
	ds_read_b32 v77, v179
	ds_read_b32 v209, v180
	ds_read_b32 v212, v181
	ds_read_b32 v213, v182
	ds_read_b32 v214, v183
	ds_read_b32 v215, v184
	ds_read_b32 v216, v185
	ds_read_b32 v217, v186
	s_waitcnt lgkmcnt(7)
	v_mul_f32_e32 v77, v70, v77
	s_waitcnt lgkmcnt(6)
	v_mul_f32_e32 v209, v71, v209
	v_cvt_pk_bf16_f32 v211, v77, v209
	s_waitcnt lgkmcnt(5)
	v_mul_f32_e32 v77, v64, v212
	s_waitcnt lgkmcnt(4)
	v_mul_f32_e32 v209, v65, v213
	v_cvt_pk_bf16_f32 v212, v77, v209
	s_waitcnt lgkmcnt(3)
	v_mul_f32_e32 v77, v66, v214
	s_waitcnt lgkmcnt(2)
	v_mul_f32_e32 v209, v67, v215
	v_cvt_pk_bf16_f32 v213, v77, v209
	v_add_u32_e32 v77, s36, v142
	v_mad_i64_i32 v[214:215], s[8:9], s31, v77, 0
	v_lshl_add_u64 v[214:215], v[214:215], 1, s[2:3]
	v_lshl_add_u64 v[214:215], v[214:215], 0, s[6:7]
	v_lshl_add_u64 v[214:215], v[214:215], 0, v[72:73]
	global_store_dwordx4 v[214:215], v[210:213], off
	s_waitcnt lgkmcnt(1)
	v_mul_f32_e32 v77, v68, v216
	s_waitcnt lgkmcnt(0)
	v_mul_f32_e32 v209, v69, v217
	v_cvt_pk_bf16_f32 v210, v77, v209
	ds_read_b32 v77, v187
	ds_read_b32 v209, v188
	ds_read_b32 v212, v189
	ds_read_b32 v213, v190
	ds_read_b32 v214, v191
	ds_read_b32 v215, v192
	ds_read_b32 v216, v193
	ds_read_b32 v217, v194
	s_waitcnt lgkmcnt(7)
	v_mul_f32_e32 v77, v70, v77
	s_waitcnt lgkmcnt(6)
	v_mul_f32_e32 v209, v71, v209
	v_cvt_pk_bf16_f32 v211, v77, v209
	s_waitcnt lgkmcnt(5)
	v_mul_f32_e32 v77, v64, v212
	s_waitcnt lgkmcnt(4)
	v_mul_f32_e32 v209, v65, v213
	v_cvt_pk_bf16_f32 v212, v77, v209
	s_waitcnt lgkmcnt(3)
	v_mul_f32_e32 v77, v66, v214
	s_waitcnt lgkmcnt(2)
	v_mul_f32_e32 v209, v67, v215
	v_cvt_pk_bf16_f32 v213, v77, v209
	v_add_u32_e32 v77, s36, v143
	v_mad_i64_i32 v[214:215], s[8:9], s31, v77, 0
	v_lshl_add_u64 v[214:215], v[214:215], 1, s[2:3]
	v_lshl_add_u64 v[214:215], v[214:215], 0, s[6:7]
	v_lshl_add_u64 v[214:215], v[214:215], 0, v[72:73]
	global_store_dwordx4 v[214:215], v[210:213], off
	s_waitcnt lgkmcnt(1)
	v_mul_f32_e32 v77, v68, v216
	s_waitcnt lgkmcnt(0)
	v_mul_f32_e32 v209, v69, v217
	v_cvt_pk_bf16_f32 v210, v77, v209
	ds_read_b32 v77, v195
	ds_read_b32 v209, v196
	ds_read_b32 v212, v197
	ds_read_b32 v213, v198
	ds_read_b32 v214, v199
	ds_read_b32 v215, v200
	ds_read_b32 v216, v201
	ds_read_b32 v217, v202
	s_waitcnt lgkmcnt(7)
	v_mul_f32_e32 v77, v70, v77
	s_waitcnt lgkmcnt(6)
	v_mul_f32_e32 v209, v71, v209
	v_cvt_pk_bf16_f32 v211, v77, v209
	s_waitcnt lgkmcnt(5)
	v_mul_f32_e32 v77, v64, v212
	s_waitcnt lgkmcnt(4)
	v_mul_f32_e32 v209, v65, v213
	v_cvt_pk_bf16_f32 v212, v77, v209
	s_waitcnt lgkmcnt(3)
	v_mul_f32_e32 v77, v66, v214
	s_waitcnt lgkmcnt(2)
	v_mul_f32_e32 v209, v67, v215
	v_cvt_pk_bf16_f32 v213, v77, v209
	v_add_u32_e32 v77, s36, v144
	v_mad_i64_i32 v[214:215], s[8:9], s31, v77, 0
	v_lshl_add_u64 v[214:215], v[214:215], 1, s[2:3]
	v_lshl_add_u64 v[214:215], v[214:215], 0, s[6:7]
	v_lshl_add_u64 v[214:215], v[214:215], 0, v[72:73]
	global_store_dwordx4 v[214:215], v[210:213], off
	ds_read_b32 v77, v203
	ds_read_b32 v209, v204
	ds_read_b32 v210, v205
	ds_read_b32 v211, v206
	ds_read_b32 v212, v207
	ds_read_b32 v213, v208
	s_waitcnt lgkmcnt(7)
	v_mul_f32_e32 v68, v68, v216
	s_waitcnt lgkmcnt(6)
	v_mul_f32_e32 v69, v69, v217
	v_cvt_pk_bf16_f32 v68, v68, v69
	s_waitcnt lgkmcnt(5)
	v_mul_f32_e32 v69, v70, v77
	s_waitcnt lgkmcnt(4)
	v_mul_f32_e32 v70, v71, v209
	s_waitcnt lgkmcnt(3)
	v_mul_f32_e32 v64, v64, v210
	v_cvt_pk_bf16_f32 v69, v69, v70
	s_waitcnt lgkmcnt(2)
	v_mul_f32_e32 v65, v65, v211
	v_cvt_pk_bf16_f32 v70, v64, v65
	s_waitcnt lgkmcnt(1)
	v_mul_f32_e32 v64, v66, v212
	s_waitcnt lgkmcnt(0)
	v_mul_f32_e32 v65, v67, v213
	v_cvt_pk_bf16_f32 v71, v64, v65
	v_add_u32_e32 v64, s36, v145
	v_mad_i64_i32 v[64:65], s[8:9], s31, v64, 0
	v_lshl_add_u64 v[64:65], v[64:65], 1, s[2:3]
	v_lshl_add_u64 v[64:65], v[64:65], 0, s[6:7]
	v_lshl_add_u64 v[64:65], v[64:65], 0, v[72:73]
	global_store_dwordx4 v[64:65], v[68:71], off
	s_waitcnt lgkmcnt(0)
	s_mov_b32 s36, s26
	s_mov_b64 s[2:3], s[14:15]
	s_mov_b64 s[6:7], s[16:17]
	s_mov_b32 s31, s58
	s_mov_b32 s8, s20
	s_cbranch_vccz .LBB0_885
	.p2align 6

.LBB0_938:
	ds_read2_b32 v[214:215], v146 offset1:32
	s_add_i32 s57, s57, s29
	s_add_i32 s28, s28, s29
	s_add_i32 s54, s54, s55
	s_add_i32 s56, s56, s44
	s_waitcnt vmcnt(0) lgkmcnt(0)
	v_mul_f32_e32 v77, v68, v214
	ds_read_b32 v209, v147
	ds_read_b32 v211, v148
	ds_read_b32 v212, v149
	ds_read_b32 v213, v150
	ds_read_b32 v214, v151
	ds_read_b32 v216, v152
	ds_read_b32 v217, v153
	ds_read_b32 v218, v154
	s_waitcnt lgkmcnt(7)
	v_mul_f32_e32 v209, v69, v209
	v_cvt_pk_bf16_f32 v210, v77, v209
	s_waitcnt lgkmcnt(6)
	v_mul_f32_e32 v77, v70, v211
	s_waitcnt lgkmcnt(5)
	v_mul_f32_e32 v209, v71, v212
	v_cvt_pk_bf16_f32 v211, v77, v209
	s_waitcnt lgkmcnt(4)
	v_mul_f32_e32 v77, v64, v213
	s_waitcnt lgkmcnt(3)
	v_mul_f32_e32 v209, v65, v214
	v_cvt_pk_bf16_f32 v212, v77, v209
	s_waitcnt lgkmcnt(2)
	v_mul_f32_e32 v77, v66, v216
	s_waitcnt lgkmcnt(1)
	v_mul_f32_e32 v209, v67, v217
	v_cvt_pk_bf16_f32 v213, v77, v209
	v_add_u32_e32 v77, s27, v138
	v_mad_i64_i32 v[216:217], s[6:7], s26, v77, 0
	v_lshl_add_u64 v[216:217], v[216:217], 1, s[2:3]
	s_lshl_b64 s[6:7], s[8:9], 1
	v_lshl_add_u64 v[216:217], v[216:217], 0, s[6:7]
	v_lshl_add_u64 v[216:217], v[216:217], 0, v[72:73]
	global_store_dwordx4 v[216:217], v[210:213], off
	s_waitcnt lgkmcnt(0)
	v_mul_f32_e32 v77, v68, v218
	ds_read_b32 v209, v155
	ds_read_b32 v211, v156
	ds_read_b32 v212, v157
	ds_read_b32 v213, v158
	ds_read_b32 v214, v159
	ds_read_b32 v216, v160
	ds_read_b32 v217, v161
	ds_read_b32 v218, v162
	s_waitcnt lgkmcnt(7)
	v_mul_f32_e32 v209, v69, v209
	v_cvt_pk_bf16_f32 v210, v77, v209
	s_waitcnt lgkmcnt(6)
	v_mul_f32_e32 v77, v70, v211
	s_waitcnt lgkmcnt(5)
	v_mul_f32_e32 v209, v71, v212
	v_cvt_pk_bf16_f32 v211, v77, v209
	s_waitcnt lgkmcnt(4)
	v_mul_f32_e32 v77, v64, v213
	s_waitcnt lgkmcnt(3)
	v_mul_f32_e32 v209, v65, v214
	v_cvt_pk_bf16_f32 v212, v77, v209
	s_waitcnt lgkmcnt(2)
	v_mul_f32_e32 v77, v66, v216
	s_waitcnt lgkmcnt(1)
	v_mul_f32_e32 v209, v67, v217
	v_cvt_pk_bf16_f32 v213, v77, v209
	v_add_u32_e32 v77, s27, v139
	v_mad_i64_i32 v[216:217], s[8:9], s26, v77, 0
	v_lshl_add_u64 v[216:217], v[216:217], 1, s[2:3]
	v_lshl_add_u64 v[216:217], v[216:217], 0, s[6:7]
	v_lshl_add_u64 v[216:217], v[216:217], 0, v[72:73]
	global_store_dwordx4 v[216:217], v[210:213], off
	s_waitcnt lgkmcnt(0)
	v_mul_f32_e32 v77, v68, v218
	ds_read_b32 v209, v163
	ds_read_b32 v211, v164
	ds_read_b32 v212, v165
	ds_read_b32 v213, v166
	ds_read_b32 v214, v167
	ds_read_b32 v216, v168
	ds_read_b32 v217, v169
	ds_read_b32 v218, v170
	s_waitcnt lgkmcnt(7)
	v_mul_f32_e32 v209, v69, v209
	v_cvt_pk_bf16_f32 v210, v77, v209
	s_waitcnt lgkmcnt(6)
	v_mul_f32_e32 v77, v70, v211
	s_waitcnt lgkmcnt(5)
	v_mul_f32_e32 v209, v71, v212
	v_cvt_pk_bf16_f32 v211, v77, v209
	s_waitcnt lgkmcnt(4)
	v_mul_f32_e32 v77, v64, v213
	s_waitcnt lgkmcnt(3)
	v_mul_f32_e32 v209, v65, v214
	v_cvt_pk_bf16_f32 v212, v77, v209
	s_waitcnt lgkmcnt(2)
	v_mul_f32_e32 v77, v66, v216
	s_waitcnt lgkmcnt(1)
	v_mul_f32_e32 v209, v67, v217
	v_cvt_pk_bf16_f32 v213, v77, v209
	v_add_u32_e32 v77, s27, v140
	v_mad_i64_i32 v[216:217], s[8:9], s26, v77, 0
	v_lshl_add_u64 v[216:217], v[216:217], 1, s[2:3]
	v_lshl_add_u64 v[216:217], v[216:217], 0, s[6:7]
	v_lshl_add_u64 v[216:217], v[216:217], 0, v[72:73]
	global_store_dwordx4 v[216:217], v[210:213], off
	s_waitcnt lgkmcnt(0)
	v_mul_f32_e32 v77, v68, v218
	ds_read_b32 v209, v171
	ds_read_b32 v211, v172
	ds_read_b32 v212, v173
	ds_read_b32 v213, v174
	ds_read_b32 v214, v175
	ds_read_b32 v216, v176
	ds_read_b32 v217, v177
	ds_read_b32 v218, v178
	s_waitcnt lgkmcnt(7)
	v_mul_f32_e32 v209, v69, v209
	v_cvt_pk_bf16_f32 v210, v77, v209
	s_waitcnt lgkmcnt(6)
	v_mul_f32_e32 v77, v70, v211
	s_waitcnt lgkmcnt(5)
	v_mul_f32_e32 v209, v71, v212
	v_cvt_pk_bf16_f32 v211, v77, v209
	s_waitcnt lgkmcnt(4)
	v_mul_f32_e32 v77, v64, v213
	s_waitcnt lgkmcnt(3)
	v_mul_f32_e32 v209, v65, v214
	v_cvt_pk_bf16_f32 v212, v77, v209
	s_waitcnt lgkmcnt(2)
	v_mul_f32_e32 v77, v66, v216
	s_waitcnt lgkmcnt(1)
	v_mul_f32_e32 v209, v67, v217
	v_cvt_pk_bf16_f32 v213, v77, v209
	v_add_u32_e32 v77, s27, v141
	v_mad_i64_i32 v[216:217], s[8:9], s26, v77, 0
	v_lshl_add_u64 v[216:217], v[216:217], 1, s[2:3]
	v_lshl_add_u64 v[216:217], v[216:217], 0, s[6:7]
	v_lshl_add_u64 v[216:217], v[216:217], 0, v[72:73]
	global_store_dwordx4 v[216:217], v[210:213], off
	v_mul_f32_e32 v77, v68, v215
	s_waitcnt lgkmcnt(0)
	v_mul_f32_e32 v209, v69, v218
	v_cvt_pk_bf16_f32 v210, v77, v209
	ds_read_b32 v77, v179
	ds_read_b32 v209, v180
	ds_read_b32 v212, v181
	ds_read_b32 v213, v182
	ds_read_b32 v214, v183
	ds_read_b32 v215, v184
	ds_read_b32 v216, v185
	ds_read_b32 v217, v186
	s_waitcnt lgkmcnt(7)
	v_mul_f32_e32 v77, v70, v77
	s_waitcnt lgkmcnt(6)
	v_mul_f32_e32 v209, v71, v209
	v_cvt_pk_bf16_f32 v211, v77, v209
	s_waitcnt lgkmcnt(5)
	v_mul_f32_e32 v77, v64, v212
	s_waitcnt lgkmcnt(4)
	v_mul_f32_e32 v209, v65, v213
	v_cvt_pk_bf16_f32 v212, v77, v209
	s_waitcnt lgkmcnt(3)
	v_mul_f32_e32 v77, v66, v214
	s_waitcnt lgkmcnt(2)
	v_mul_f32_e32 v209, v67, v215
	v_cvt_pk_bf16_f32 v213, v77, v209
	v_add_u32_e32 v77, s27, v142
	v_mad_i64_i32 v[214:215], s[8:9], s26, v77, 0
	v_lshl_add_u64 v[214:215], v[214:215], 1, s[2:3]
	v_lshl_add_u64 v[214:215], v[214:215], 0, s[6:7]
	v_lshl_add_u64 v[214:215], v[214:215], 0, v[72:73]
	global_store_dwordx4 v[214:215], v[210:213], off
	s_waitcnt lgkmcnt(1)
	v_mul_f32_e32 v77, v68, v216
	s_waitcnt lgkmcnt(0)
	v_mul_f32_e32 v209, v69, v217
	v_cvt_pk_bf16_f32 v210, v77, v209
	ds_read_b32 v77, v187
	ds_read_b32 v209, v188
	ds_read_b32 v212, v189
	ds_read_b32 v213, v190
	ds_read_b32 v214, v191
	ds_read_b32 v215, v192
	ds_read_b32 v216, v193
	ds_read_b32 v217, v194
	s_waitcnt lgkmcnt(7)
	v_mul_f32_e32 v77, v70, v77
	s_waitcnt lgkmcnt(6)
	v_mul_f32_e32 v209, v71, v209
	v_cvt_pk_bf16_f32 v211, v77, v209
	s_waitcnt lgkmcnt(5)
	v_mul_f32_e32 v77, v64, v212
	s_waitcnt lgkmcnt(4)
	v_mul_f32_e32 v209, v65, v213
	v_cvt_pk_bf16_f32 v212, v77, v209
	s_waitcnt lgkmcnt(3)
	v_mul_f32_e32 v77, v66, v214
	s_waitcnt lgkmcnt(2)
	v_mul_f32_e32 v209, v67, v215
	v_cvt_pk_bf16_f32 v213, v77, v209
	v_add_u32_e32 v77, s27, v143
	v_mad_i64_i32 v[214:215], s[8:9], s26, v77, 0
	v_lshl_add_u64 v[214:215], v[214:215], 1, s[2:3]
	v_lshl_add_u64 v[214:215], v[214:215], 0, s[6:7]
	v_lshl_add_u64 v[214:215], v[214:215], 0, v[72:73]
	global_store_dwordx4 v[214:215], v[210:213], off
	s_waitcnt lgkmcnt(1)
	v_mul_f32_e32 v77, v68, v216
	s_waitcnt lgkmcnt(0)
	v_mul_f32_e32 v209, v69, v217
	v_cvt_pk_bf16_f32 v210, v77, v209
	ds_read_b32 v77, v195
	ds_read_b32 v209, v196
	ds_read_b32 v212, v197
	ds_read_b32 v213, v198
	ds_read_b32 v214, v199
	ds_read_b32 v215, v200
	ds_read_b32 v216, v201
	ds_read_b32 v217, v202
	s_waitcnt lgkmcnt(7)
	v_mul_f32_e32 v77, v70, v77
	s_waitcnt lgkmcnt(6)
	v_mul_f32_e32 v209, v71, v209
	v_cvt_pk_bf16_f32 v211, v77, v209
	s_waitcnt lgkmcnt(5)
	v_mul_f32_e32 v77, v64, v212
	s_waitcnt lgkmcnt(4)
	v_mul_f32_e32 v209, v65, v213
	v_cvt_pk_bf16_f32 v212, v77, v209
	s_waitcnt lgkmcnt(3)
	v_mul_f32_e32 v77, v66, v214
	s_waitcnt lgkmcnt(2)
	v_mul_f32_e32 v209, v67, v215
	v_cvt_pk_bf16_f32 v213, v77, v209
	v_add_u32_e32 v77, s27, v144
	v_mad_i64_i32 v[214:215], s[8:9], s26, v77, 0
	v_lshl_add_u64 v[214:215], v[214:215], 1, s[2:3]
	v_lshl_add_u64 v[214:215], v[214:215], 0, s[6:7]
	v_lshl_add_u64 v[214:215], v[214:215], 0, v[72:73]
	global_store_dwordx4 v[214:215], v[210:213], off
	ds_read_b32 v77, v203
	ds_read_b32 v209, v204
	ds_read_b32 v210, v205
	ds_read_b32 v211, v206
	ds_read_b32 v212, v207
	ds_read_b32 v213, v208
	s_waitcnt lgkmcnt(7)
	v_mul_f32_e32 v68, v68, v216
	s_waitcnt lgkmcnt(6)
	v_mul_f32_e32 v69, v69, v217
	v_cvt_pk_bf16_f32 v68, v68, v69
	s_waitcnt lgkmcnt(5)
	v_mul_f32_e32 v69, v70, v77
	s_waitcnt lgkmcnt(4)
	v_mul_f32_e32 v70, v71, v209
	s_waitcnt lgkmcnt(3)
	v_mul_f32_e32 v64, v64, v210
	v_cvt_pk_bf16_f32 v69, v69, v70
	s_waitcnt lgkmcnt(2)
	v_mul_f32_e32 v65, v65, v211
	v_cvt_pk_bf16_f32 v70, v64, v65
	s_waitcnt lgkmcnt(1)
	v_mul_f32_e32 v64, v66, v212
	s_waitcnt lgkmcnt(0)
	v_mul_f32_e32 v65, v67, v213
	v_cvt_pk_bf16_f32 v71, v64, v65
	v_add_u32_e32 v64, s27, v145
	v_mad_i64_i32 v[64:65], s[8:9], s26, v64, 0
	v_lshl_add_u64 v[64:65], v[64:65], 1, s[2:3]
	v_lshl_add_u64 v[64:65], v[64:65], 0, s[6:7]
	v_lshl_add_u64 v[64:65], v[64:65], 0, v[72:73]
	global_store_dwordx4 v[64:65], v[68:71], off
	s_waitcnt lgkmcnt(0)
	s_add_i32 s2, s53, s57
	s_cmpk_gt_i32 s2, 0x13ff
	s_mov_b32 s27, s24
	s_mov_b64 s[2:3], s[12:13]
	s_mov_b64 s[6:7], s[14:15]
	s_mov_b32 s26, s58
	s_mov_b32 s8, s18
	s_cbranch_scc1 .LBB0_972
	.p2align 6

.LBB0_1038:
	s_cmp_gt_i32 s34, 12
	s_cselect_b64 s[2:3], -1, 0
	s_cmp_lt_i32 s35, 13
	s_cselect_b64 s[4:5], -1, 0
	s_or_b64 s[2:3], s[2:3], s[4:5]
	s_and_b64 vcc, exec, s[2:3]
	s_cbranch_vccnz .LBB0_1157
	s_mov_b32 s2, 24
	s_lshl_b32 s2, s2, 3
	s_add_i32 s2, s2, 0
	s_add_i32 s2, s2, 0x201c0
	v_mov_b32_e32 v0, s2
	s_waitcnt vmcnt(0) lgkmcnt(0)
	ds_read_b32 v1, v0
	ds_read_b32 v0, v0 offset:4
	s_and_b32 s40, s33, 0xffffffc0
	v_mbcnt_lo_u32_b32 v2, -1, 0
	v_mbcnt_hi_u32_b32 v2, -1, v2
	s_waitcnt lgkmcnt(1)
	v_readfirstlane_b32 s18, v1
	s_waitcnt lgkmcnt(0)
	v_readfirstlane_b32 s19, v0
	v_add_u32_e32 v0, s40, v2
	v_cmp_gt_i32_e32 vcc, 64, v0
	s_and_saveexec_b64 s[2:3], vcc
	s_cbranch_execz .LBB0_1055
	v_lshlrev_b32_e32 v2, 5, v0
	v_ashrrev_i32_e32 v3, 31, v2
	v_lshl_add_u64 v[2:3], v[2:3], 2, s[18:19]
	v_add_co_u32_e32 v2, vcc, 0x8000, v2
	v_lshlrev_b32_e32 v9, 2, v0
	s_nop 0
	v_addc_co_u32_e32 v3, vcc, 0, v3, vcc
	global_load_dword v8, v[2:3], off sc1
	v_add_u32_e32 v1, -4, v9
	v_cmp_lt_i32_e32 vcc, 0, v0
	v_add_u32_e32 v4, -8, v9
	v_add_u32_e32 v5, -16, v9
	v_subrev_u32_e32 v6, 32, v9
	v_subrev_u32_e32 v7, 64, v9
	v_add_u32_e32 v10, 0xffffff80, v9
	v_add_u32_e32 v9, 0, v9
	v_add_u32_e32 v9, 0x20a00, v9
	s_waitcnt vmcnt(0)
	v_add_u32_e32 v2, 0xff, v8
	v_ashrrev_i32_e32 v2, 8, v2
	ds_bpermute_b32 v1, v1, v2
	ds_write_b32 v9, v8
	s_waitcnt lgkmcnt(1)
	v_cndmask_b32_e32 v3, 0, v1, vcc
	v_add_u32_e32 v1, v3, v2
	ds_bpermute_b32 v4, v4, v1
	v_cmp_lt_i32_e32 vcc, 1, v0
	s_waitcnt lgkmcnt(0)
	s_nop 0
	v_cndmask_b32_e32 v4, 0, v4, vcc
	v_add_u32_e32 v1, v4, v1
	ds_bpermute_b32 v5, v5, v1
	v_cmp_lt_i32_e32 vcc, 3, v0
	s_waitcnt lgkmcnt(0)
	s_nop 0
	v_cndmask_b32_e32 v5, 0, v5, vcc
	v_add_u32_e32 v1, v5, v1
	ds_bpermute_b32 v6, v6, v1
	v_cmp_lt_i32_e32 vcc, 7, v0
	s_waitcnt lgkmcnt(0)
	s_nop 0
	v_cndmask_b32_e32 v6, 0, v6, vcc
	v_add_u32_e32 v1, v6, v1
	ds_bpermute_b32 v7, v7, v1
	v_cmp_lt_i32_e32 vcc, 15, v0
	s_waitcnt lgkmcnt(0)
	s_nop 0
	v_cndmask_b32_e32 v7, 0, v7, vcc
	v_add_u32_e32 v1, v7, v1
	ds_bpermute_b32 v10, v10, v1
	v_cmp_lt_i32_e32 vcc, 31, v0
	s_waitcnt lgkmcnt(0)
	s_nop 0
	v_cndmask_b32_e32 v9, 0, v10, vcc
	v_cmp_eq_u32_e32 vcc, 63, v0
	s_and_saveexec_b64 s[4:5], vcc
	s_add_i32 s6, 0, 0x20b00
	v_add_u32_e32 v1, v9, v1
	v_mov_b32_e32 v8, s6
	ds_write_b32 v8, v1
	s_or_b64 exec, exec, s[4:5]
	v_cmp_lt_i32_e32 vcc, 0, v2
	s_and_b64 exec, exec, vcc
	s_cbranch_execz .LBB0_1055
	v_lshlrev_b32_e32 v8, 16, v0
	v_cmp_ne_u32_e32 vcc, 1, v2
	s_mov_b64 s[6:7], -1
	v_mov_b32_e32 v0, 0
	s_and_saveexec_b64 s[4:5], vcc
	s_cbranch_execz .LBB0_1052
	v_add_u32_e32 v0, -2, v2
	v_lshrrev_b32_e32 v1, 1, v0
	v_cmp_lt_u32_e32 vcc, 13, v0
	v_mov_b32_e32 v0, 0
	v_add_u32_e32 v10, 1, v1
	s_mov_b32 s14, 0
	v_mov_b32_e32 v1, 1
	v_mov_b32_e32 v13, v0
	s_and_saveexec_b64 s[6:7], vcc
	s_cbranch_execz .LBB0_1048
	v_add_u32_e32 v0, v3, v4
	v_add3_u32 v0, v0, v5, v6
	v_add3_u32 v0, v0, v7, v9
	v_lshl_add_u32 v0, v0, 2, 0
	v_and_b32_e32 v11, -8, v10
	v_add_u32_e32 v12, 0x20400, v0
	s_mov_b32 s13, 1
	s_mov_b64 s[8:9], 0
	s_mov_b32 s12, 0
	.p2align 6

.LBB0_1048:
	s_or_b64 exec, exec, s[6:7]
	v_and_b32_e32 v10, 7, v10
	v_cmp_ne_u32_e32 vcc, 0, v10
	s_and_saveexec_b64 s[6:7], vcc
	s_cbranch_execz .LBB0_1051
	v_add3_u32 v12, v3, v4, v5
	v_add3_u32 v12, v12, v6, v7
	v_lshlrev_b32_e32 v11, 2, v13
	v_add_lshl_u32 v12, v12, v9, 2
	v_add3_u32 v11, v11, v12, 0
	v_add_u32_e32 v11, 0x20400, v11
	s_mov_b64 s[8:9], 0
	.p2align 6

.LBB0_1052:
	s_or_b64 exec, exec, s[4:5]
	s_and_b64 exec, exec, s[6:7]
	s_cbranch_execz .LBB0_1055
	v_add3_u32 v3, v3, v4, v5
	v_add3_u32 v3, v3, v6, v7
	v_lshlrev_b32_e32 v1, 2, v0
	v_add_lshl_u32 v3, v3, v9, 2
	v_add3_u32 v1, v1, v3, 0
	v_add_u32_e32 v1, 0x20400, v1
	s_mov_b64 s[4:5], 0
	.p2align 6

.LBB0_1065:
	s_and_b64 vcc, exec, s[30:31]
	s_mov_b32 s52, s66
	s_mov_b32 s49, s65
	s_mov_b32 s67, s64
	s_mov_b64 s[38:39], s[28:29]
	s_mov_b64 s[36:37], s[26:27]
	s_cbranch_vccnz .LBB0_1089
	.p2align 6

.LBB0_1163:
	s_or_b64 exec, exec, s[22:23]
	s_add_i32 s12, s12, s14
	s_add_i32 s16, s16, s25
	s_add_u32 s26, s26, s18
	s_addc_u32 s27, s27, s19
	s_cmp_lt_i32 s12, 0x8000
	v_lshl_add_u64 v[4:5], v[4:5], 0, s[20:21]
	s_cbranch_scc0 .LBB0_1166
	.p2align 6

.LBB0_1242:
	s_add_u32 s19, s30, 0x100
	v_mov_b32_e32 v0, 0
	s_addc_u32 s21, s31, 0
	s_mov_b32 s61, -2
	v_mov_b32_e32 v1, v0
	v_mov_b32_e32 v2, v0
	v_mov_b32_e32 v3, v0
	v_mov_b32_e32 v4, v0
	v_mov_b32_e32 v5, v0
	v_mov_b32_e32 v6, v0
	v_mov_b32_e32 v7, v0
	v_mov_b32_e32 v12, v0
	v_mov_b32_e32 v13, v0
	v_mov_b32_e32 v14, v0
	v_mov_b32_e32 v15, v0
	v_mov_b32_e32 v20, v0
	v_mov_b32_e32 v21, v0
	v_mov_b32_e32 v22, v0
	v_mov_b32_e32 v23, v0
	v_mov_b32_e32 v28, v0
	v_mov_b32_e32 v29, v0
	v_mov_b32_e32 v30, v0
	v_mov_b32_e32 v31, v0
	v_mov_b32_e32 v36, v0
	v_mov_b32_e32 v37, v0
	v_mov_b32_e32 v38, v0
	v_mov_b32_e32 v39, v0
	v_mov_b32_e32 v44, v0
	v_mov_b32_e32 v45, v0
	v_mov_b32_e32 v46, v0
	v_mov_b32_e32 v47, v0
	v_mov_b32_e32 v52, v0
	v_mov_b32_e32 v53, v0
	v_mov_b32_e32 v54, v0
	v_mov_b32_e32 v55, v0
	v_mov_b32_e32 v8, v0
	v_mov_b32_e32 v9, v0
	v_mov_b32_e32 v10, v0
	v_mov_b32_e32 v11, v0
	v_mov_b32_e32 v16, v0
	v_mov_b32_e32 v17, v0
	v_mov_b32_e32 v18, v0
	v_mov_b32_e32 v19, v0
	v_mov_b32_e32 v24, v0
	v_mov_b32_e32 v25, v0
	v_mov_b32_e32 v26, v0
	v_mov_b32_e32 v27, v0
	v_mov_b32_e32 v32, v0
	v_mov_b32_e32 v33, v0
	v_mov_b32_e32 v34, v0
	v_mov_b32_e32 v35, v0
	v_mov_b32_e32 v40, v0
	v_mov_b32_e32 v41, v0
	v_mov_b32_e32 v42, v0
	v_mov_b32_e32 v43, v0
	v_mov_b32_e32 v48, v0
	v_mov_b32_e32 v49, v0
	v_mov_b32_e32 v50, v0
	v_mov_b32_e32 v51, v0
	v_mov_b32_e32 v56, v0
	v_mov_b32_e32 v57, v0
	v_mov_b32_e32 v58, v0
	v_mov_b32_e32 v59, v0
	v_mov_b32_e32 v60, v0
	v_mov_b32_e32 v61, v0
	v_mov_b32_e32 v62, v0
	v_mov_b32_e32 v63, v0
	v_mov_b32_e32 v64, v0
	v_mov_b32_e32 v65, v0
	v_mov_b32_e32 v66, v0
	v_mov_b32_e32 v67, v0
	v_mov_b32_e32 v68, v0
	v_mov_b32_e32 v69, v0
	v_mov_b32_e32 v70, v0
	v_mov_b32_e32 v71, v0
	v_mov_b32_e32 v72, v0
	v_mov_b32_e32 v73, v0
	v_mov_b32_e32 v74, v0
	v_mov_b32_e32 v75, v0
	v_mov_b32_e32 v76, v0
	v_mov_b32_e32 v77, v0
	v_mov_b32_e32 v78, v0
	v_mov_b32_e32 v79, v0
	v_mov_b32_e32 v84, v0
	v_mov_b32_e32 v85, v0
	v_mov_b32_e32 v86, v0
	v_mov_b32_e32 v87, v0
	v_mov_b32_e32 v88, v0
	v_mov_b32_e32 v89, v0
	v_mov_b32_e32 v90, v0
	v_mov_b32_e32 v91, v0
	v_mov_b32_e32 v96, v0
	v_mov_b32_e32 v97, v0
	v_mov_b32_e32 v98, v0
	v_mov_b32_e32 v99, v0
	v_mov_b32_e32 v104, v0
	v_mov_b32_e32 v105, v0
	v_mov_b32_e32 v106, v0
	v_mov_b32_e32 v107, v0
	v_mov_b32_e32 v80, v0
	v_mov_b32_e32 v81, v0
	v_mov_b32_e32 v82, v0
	v_mov_b32_e32 v83, v0
	v_mov_b32_e32 v92, v0
	v_mov_b32_e32 v93, v0
	v_mov_b32_e32 v94, v0
	v_mov_b32_e32 v95, v0
	v_mov_b32_e32 v100, v0
	v_mov_b32_e32 v101, v0
	v_mov_b32_e32 v102, v0
	v_mov_b32_e32 v103, v0
	v_mov_b32_e32 v108, v0
	v_mov_b32_e32 v109, v0
	v_mov_b32_e32 v110, v0
	v_mov_b32_e32 v111, v0
	v_mov_b32_e32 v112, v0
	v_mov_b32_e32 v113, v0
	v_mov_b32_e32 v114, v0
	v_mov_b32_e32 v115, v0
	v_mov_b32_e32 v116, v0
	v_mov_b32_e32 v117, v0
	v_mov_b32_e32 v118, v0
	v_mov_b32_e32 v119, v0
	v_mov_b32_e32 v120, v0
	v_mov_b32_e32 v121, v0
	v_mov_b32_e32 v122, v0
	v_mov_b32_e32 v123, v0
	v_mov_b32_e32 v124, v0
	v_mov_b32_e32 v125, v0
	v_mov_b32_e32 v126, v0
	v_mov_b32_e32 v127, v0
	.p2align 6

.LBB0_1295:
	ds_read2_b32 v[214:215], v146 offset1:32
	s_addk_i32 s26, 0x400
	s_addk_i32 s51, 0x400
	s_add_i32 s52, s52, 0x10000
	s_waitcnt vmcnt(0) lgkmcnt(0)
	v_mul_f32_e32 v77, v68, v214
	ds_read_b32 v209, v147
	ds_read_b32 v211, v148
	ds_read_b32 v212, v149
	ds_read_b32 v213, v150
	ds_read_b32 v214, v151
	ds_read_b32 v216, v152
	ds_read_b32 v217, v153
	ds_read_b32 v218, v154
	s_waitcnt lgkmcnt(7)
	v_mul_f32_e32 v209, v69, v209
	v_cvt_pk_bf16_f32 v210, v77, v209
	s_waitcnt lgkmcnt(6)
	v_mul_f32_e32 v77, v70, v211
	s_waitcnt lgkmcnt(5)
	v_mul_f32_e32 v209, v71, v212
	v_cvt_pk_bf16_f32 v211, v77, v209
	s_waitcnt lgkmcnt(4)
	v_mul_f32_e32 v77, v64, v213
	s_waitcnt lgkmcnt(3)
	v_mul_f32_e32 v209, v65, v214
	v_cvt_pk_bf16_f32 v212, v77, v209
	s_waitcnt lgkmcnt(2)
	v_mul_f32_e32 v77, v66, v216
	s_waitcnt lgkmcnt(1)
	v_mul_f32_e32 v209, v67, v217
	v_cvt_pk_bf16_f32 v213, v77, v209
	v_add_u32_e32 v77, s28, v138
	v_mad_i64_i32 v[216:217], s[6:7], s27, v77, 0
	v_lshl_add_u64 v[216:217], v[216:217], 1, s[2:3]
	s_lshl_b64 s[6:7], s[8:9], 1
	v_lshl_add_u64 v[216:217], v[216:217], 0, s[6:7]
	v_lshl_add_u64 v[216:217], v[216:217], 0, v[72:73]
	global_store_dwordx4 v[216:217], v[210:213], off
	s_waitcnt lgkmcnt(0)
	v_mul_f32_e32 v77, v68, v218
	ds_read_b32 v209, v155
	ds_read_b32 v211, v156
	ds_read_b32 v212, v157
	ds_read_b32 v213, v158
	ds_read_b32 v214, v159
	ds_read_b32 v216, v160
	ds_read_b32 v217, v161
	ds_read_b32 v218, v162
	s_waitcnt lgkmcnt(7)
	v_mul_f32_e32 v209, v69, v209
	v_cvt_pk_bf16_f32 v210, v77, v209
	s_waitcnt lgkmcnt(6)
	v_mul_f32_e32 v77, v70, v211
	s_waitcnt lgkmcnt(5)
	v_mul_f32_e32 v209, v71, v212
	v_cvt_pk_bf16_f32 v211, v77, v209
	s_waitcnt lgkmcnt(4)
	v_mul_f32_e32 v77, v64, v213
	s_waitcnt lgkmcnt(3)
	v_mul_f32_e32 v209, v65, v214
	v_cvt_pk_bf16_f32 v212, v77, v209
	s_waitcnt lgkmcnt(2)
	v_mul_f32_e32 v77, v66, v216
	s_waitcnt lgkmcnt(1)
	v_mul_f32_e32 v209, v67, v217
	v_cvt_pk_bf16_f32 v213, v77, v209
	v_add_u32_e32 v77, s28, v139
	v_mad_i64_i32 v[216:217], s[8:9], s27, v77, 0
	v_lshl_add_u64 v[216:217], v[216:217], 1, s[2:3]
	v_lshl_add_u64 v[216:217], v[216:217], 0, s[6:7]
	v_lshl_add_u64 v[216:217], v[216:217], 0, v[72:73]
	global_store_dwordx4 v[216:217], v[210:213], off
	s_waitcnt lgkmcnt(0)
	v_mul_f32_e32 v77, v68, v218
	ds_read_b32 v209, v163
	ds_read_b32 v211, v164
	ds_read_b32 v212, v165
	ds_read_b32 v213, v166
	ds_read_b32 v214, v167
	ds_read_b32 v216, v168
	ds_read_b32 v217, v169
	ds_read_b32 v218, v170
	s_waitcnt lgkmcnt(7)
	v_mul_f32_e32 v209, v69, v209
	v_cvt_pk_bf16_f32 v210, v77, v209
	s_waitcnt lgkmcnt(6)
	v_mul_f32_e32 v77, v70, v211
	s_waitcnt lgkmcnt(5)
	v_mul_f32_e32 v209, v71, v212
	v_cvt_pk_bf16_f32 v211, v77, v209
	s_waitcnt lgkmcnt(4)
	v_mul_f32_e32 v77, v64, v213
	s_waitcnt lgkmcnt(3)
	v_mul_f32_e32 v209, v65, v214
	v_cvt_pk_bf16_f32 v212, v77, v209
	s_waitcnt lgkmcnt(2)
	v_mul_f32_e32 v77, v66, v216
	s_waitcnt lgkmcnt(1)
	v_mul_f32_e32 v209, v67, v217
	v_cvt_pk_bf16_f32 v213, v77, v209
	v_add_u32_e32 v77, s28, v140
	v_mad_i64_i32 v[216:217], s[8:9], s27, v77, 0
	v_lshl_add_u64 v[216:217], v[216:217], 1, s[2:3]
	v_lshl_add_u64 v[216:217], v[216:217], 0, s[6:7]
	v_lshl_add_u64 v[216:217], v[216:217], 0, v[72:73]
	global_store_dwordx4 v[216:217], v[210:213], off
	s_waitcnt lgkmcnt(0)
	v_mul_f32_e32 v77, v68, v218
	ds_read_b32 v209, v171
	ds_read_b32 v211, v172
	ds_read_b32 v212, v173
	ds_read_b32 v213, v174
	ds_read_b32 v214, v175
	ds_read_b32 v216, v176
	ds_read_b32 v217, v177
	ds_read_b32 v218, v178
	s_waitcnt lgkmcnt(7)
	v_mul_f32_e32 v209, v69, v209
	v_cvt_pk_bf16_f32 v210, v77, v209
	s_waitcnt lgkmcnt(6)
	v_mul_f32_e32 v77, v70, v211
	s_waitcnt lgkmcnt(5)
	v_mul_f32_e32 v209, v71, v212
	v_cvt_pk_bf16_f32 v211, v77, v209
	s_waitcnt lgkmcnt(4)
	v_mul_f32_e32 v77, v64, v213
	s_waitcnt lgkmcnt(3)
	v_mul_f32_e32 v209, v65, v214
	v_cvt_pk_bf16_f32 v212, v77, v209
	s_waitcnt lgkmcnt(2)
	v_mul_f32_e32 v77, v66, v216
	s_waitcnt lgkmcnt(1)
	v_mul_f32_e32 v209, v67, v217
	v_cvt_pk_bf16_f32 v213, v77, v209
	v_add_u32_e32 v77, s28, v141
	v_mad_i64_i32 v[216:217], s[8:9], s27, v77, 0
	v_lshl_add_u64 v[216:217], v[216:217], 1, s[2:3]
	v_lshl_add_u64 v[216:217], v[216:217], 0, s[6:7]
	v_lshl_add_u64 v[216:217], v[216:217], 0, v[72:73]
	global_store_dwordx4 v[216:217], v[210:213], off
	v_mul_f32_e32 v77, v68, v215
	s_waitcnt lgkmcnt(0)
	v_mul_f32_e32 v209, v69, v218
	v_cvt_pk_bf16_f32 v210, v77, v209
	ds_read_b32 v77, v179
	ds_read_b32 v209, v180
	ds_read_b32 v212, v181
	ds_read_b32 v213, v182
	ds_read_b32 v214, v183
	ds_read_b32 v215, v184
	ds_read_b32 v216, v185
	ds_read_b32 v217, v186
	s_waitcnt lgkmcnt(7)
	v_mul_f32_e32 v77, v70, v77
	s_waitcnt lgkmcnt(6)
	v_mul_f32_e32 v209, v71, v209
	v_cvt_pk_bf16_f32 v211, v77, v209
	s_waitcnt lgkmcnt(5)
	v_mul_f32_e32 v77, v64, v212
	s_waitcnt lgkmcnt(4)
	v_mul_f32_e32 v209, v65, v213
	v_cvt_pk_bf16_f32 v212, v77, v209
	s_waitcnt lgkmcnt(3)
	v_mul_f32_e32 v77, v66, v214
	s_waitcnt lgkmcnt(2)
	v_mul_f32_e32 v209, v67, v215
	v_cvt_pk_bf16_f32 v213, v77, v209
	v_add_u32_e32 v77, s28, v142
	v_mad_i64_i32 v[214:215], s[8:9], s27, v77, 0
	v_lshl_add_u64 v[214:215], v[214:215], 1, s[2:3]
	v_lshl_add_u64 v[214:215], v[214:215], 0, s[6:7]
	v_lshl_add_u64 v[214:215], v[214:215], 0, v[72:73]
	global_store_dwordx4 v[214:215], v[210:213], off
	s_waitcnt lgkmcnt(1)
	v_mul_f32_e32 v77, v68, v216
	s_waitcnt lgkmcnt(0)
	v_mul_f32_e32 v209, v69, v217
	v_cvt_pk_bf16_f32 v210, v77, v209
	ds_read_b32 v77, v187
	ds_read_b32 v209, v188
	ds_read_b32 v212, v189
	ds_read_b32 v213, v190
	ds_read_b32 v214, v191
	ds_read_b32 v215, v192
	ds_read_b32 v216, v193
	ds_read_b32 v217, v194
	s_waitcnt lgkmcnt(7)
	v_mul_f32_e32 v77, v70, v77
	s_waitcnt lgkmcnt(6)
	v_mul_f32_e32 v209, v71, v209
	v_cvt_pk_bf16_f32 v211, v77, v209
	s_waitcnt lgkmcnt(5)
	v_mul_f32_e32 v77, v64, v212
	s_waitcnt lgkmcnt(4)
	v_mul_f32_e32 v209, v65, v213
	v_cvt_pk_bf16_f32 v212, v77, v209
	s_waitcnt lgkmcnt(3)
	v_mul_f32_e32 v77, v66, v214
	s_waitcnt lgkmcnt(2)
	v_mul_f32_e32 v209, v67, v215
	v_cvt_pk_bf16_f32 v213, v77, v209
	v_add_u32_e32 v77, s28, v143
	v_mad_i64_i32 v[214:215], s[8:9], s27, v77, 0
	v_lshl_add_u64 v[214:215], v[214:215], 1, s[2:3]
	v_lshl_add_u64 v[214:215], v[214:215], 0, s[6:7]
	v_lshl_add_u64 v[214:215], v[214:215], 0, v[72:73]
	global_store_dwordx4 v[214:215], v[210:213], off
	s_waitcnt lgkmcnt(1)
	v_mul_f32_e32 v77, v68, v216
	s_waitcnt lgkmcnt(0)
	v_mul_f32_e32 v209, v69, v217
	v_cvt_pk_bf16_f32 v210, v77, v209
	ds_read_b32 v77, v195
	ds_read_b32 v209, v196
	ds_read_b32 v212, v197
	ds_read_b32 v213, v198
	ds_read_b32 v214, v199
	ds_read_b32 v215, v200
	ds_read_b32 v216, v201
	ds_read_b32 v217, v202
	s_waitcnt lgkmcnt(7)
	v_mul_f32_e32 v77, v70, v77
	s_waitcnt lgkmcnt(6)
	v_mul_f32_e32 v209, v71, v209
	v_cvt_pk_bf16_f32 v211, v77, v209
	s_waitcnt lgkmcnt(5)
	v_mul_f32_e32 v77, v64, v212
	s_waitcnt lgkmcnt(4)
	v_mul_f32_e32 v209, v65, v213
	v_cvt_pk_bf16_f32 v212, v77, v209
	s_waitcnt lgkmcnt(3)
	v_mul_f32_e32 v77, v66, v214
	s_waitcnt lgkmcnt(2)
	v_mul_f32_e32 v209, v67, v215
	v_cvt_pk_bf16_f32 v213, v77, v209
	v_add_u32_e32 v77, s28, v144
	v_mad_i64_i32 v[214:215], s[8:9], s27, v77, 0
	v_lshl_add_u64 v[214:215], v[214:215], 1, s[2:3]
	v_lshl_add_u64 v[214:215], v[214:215], 0, s[6:7]
	v_lshl_add_u64 v[214:215], v[214:215], 0, v[72:73]
	global_store_dwordx4 v[214:215], v[210:213], off
	ds_read_b32 v77, v203
	ds_read_b32 v209, v204
	ds_read_b32 v210, v205
	ds_read_b32 v211, v206
	ds_read_b32 v212, v207
	ds_read_b32 v213, v208
	s_waitcnt lgkmcnt(7)
	v_mul_f32_e32 v68, v68, v216
	s_waitcnt lgkmcnt(6)
	v_mul_f32_e32 v69, v69, v217
	v_cvt_pk_bf16_f32 v68, v68, v69
	s_waitcnt lgkmcnt(5)
	v_mul_f32_e32 v69, v70, v77
	s_waitcnt lgkmcnt(4)
	v_mul_f32_e32 v70, v71, v209
	s_waitcnt lgkmcnt(3)
	v_mul_f32_e32 v64, v64, v210
	v_cvt_pk_bf16_f32 v69, v69, v70
	s_waitcnt lgkmcnt(2)
	v_mul_f32_e32 v65, v65, v211
	v_cvt_pk_bf16_f32 v70, v64, v65
	s_waitcnt lgkmcnt(1)
	v_mul_f32_e32 v64, v66, v212
	s_waitcnt lgkmcnt(0)
	v_mul_f32_e32 v65, v67, v213
	v_cvt_pk_bf16_f32 v71, v64, v65
	v_add_u32_e32 v64, s28, v145
	v_mad_i64_i32 v[64:65], s[8:9], s27, v64, 0
	v_lshl_add_u64 v[64:65], v[64:65], 1, s[2:3]
	v_lshl_add_u64 v[64:65], v[64:65], 0, s[6:7]
	v_lshl_add_u64 v[64:65], v[64:65], 0, v[72:73]
	global_store_dwordx4 v[64:65], v[68:71], off
	s_waitcnt lgkmcnt(0)
	s_cmpk_lt_i32 s53, 0x800
	s_mov_b32 s28, s24
	s_mov_b64 s[2:3], s[12:13]
	s_mov_b64 s[6:7], s[14:15]
	s_mov_b32 s27, s54
	s_mov_b32 s8, s18
	s_cbranch_scc0 .LBB0_1329
	.p2align 6

.LBB0_1404:
	s_add_u32 s59, s22, 0x100
	v_mov_b32_e32 v0, 0
	s_addc_u32 s60, s23, 0
	s_mov_b32 s61, -2
	v_mov_b32_e32 v1, v0
	v_mov_b32_e32 v2, v0
	v_mov_b32_e32 v3, v0
	v_mov_b32_e32 v4, v0
	v_mov_b32_e32 v5, v0
	v_mov_b32_e32 v6, v0
	v_mov_b32_e32 v7, v0
	v_mov_b32_e32 v12, v0
	v_mov_b32_e32 v13, v0
	v_mov_b32_e32 v14, v0
	v_mov_b32_e32 v15, v0
	v_mov_b32_e32 v20, v0
	v_mov_b32_e32 v21, v0
	v_mov_b32_e32 v22, v0
	v_mov_b32_e32 v23, v0
	v_mov_b32_e32 v28, v0
	v_mov_b32_e32 v29, v0
	v_mov_b32_e32 v30, v0
	v_mov_b32_e32 v31, v0
	v_mov_b32_e32 v36, v0
	v_mov_b32_e32 v37, v0
	v_mov_b32_e32 v38, v0
	v_mov_b32_e32 v39, v0
	v_mov_b32_e32 v44, v0
	v_mov_b32_e32 v45, v0
	v_mov_b32_e32 v46, v0
	v_mov_b32_e32 v47, v0
	v_mov_b32_e32 v52, v0
	v_mov_b32_e32 v53, v0
	v_mov_b32_e32 v54, v0
	v_mov_b32_e32 v55, v0
	v_mov_b32_e32 v8, v0
	v_mov_b32_e32 v9, v0
	v_mov_b32_e32 v10, v0
	v_mov_b32_e32 v11, v0
	v_mov_b32_e32 v16, v0
	v_mov_b32_e32 v17, v0
	v_mov_b32_e32 v18, v0
	v_mov_b32_e32 v19, v0
	v_mov_b32_e32 v24, v0
	v_mov_b32_e32 v25, v0
	v_mov_b32_e32 v26, v0
	v_mov_b32_e32 v27, v0
	v_mov_b32_e32 v32, v0
	v_mov_b32_e32 v33, v0
	v_mov_b32_e32 v34, v0
	v_mov_b32_e32 v35, v0
	v_mov_b32_e32 v40, v0
	v_mov_b32_e32 v41, v0
	v_mov_b32_e32 v42, v0
	v_mov_b32_e32 v43, v0
	v_mov_b32_e32 v48, v0
	v_mov_b32_e32 v49, v0
	v_mov_b32_e32 v50, v0
	v_mov_b32_e32 v51, v0
	v_mov_b32_e32 v56, v0
	v_mov_b32_e32 v57, v0
	v_mov_b32_e32 v58, v0
	v_mov_b32_e32 v59, v0
	v_mov_b32_e32 v60, v0
	v_mov_b32_e32 v61, v0
	v_mov_b32_e32 v62, v0
	v_mov_b32_e32 v63, v0
	v_mov_b32_e32 v64, v0
	v_mov_b32_e32 v65, v0
	v_mov_b32_e32 v66, v0
	v_mov_b32_e32 v67, v0
	v_mov_b32_e32 v68, v0
	v_mov_b32_e32 v69, v0
	v_mov_b32_e32 v70, v0
	v_mov_b32_e32 v71, v0
	v_mov_b32_e32 v76, v0
	v_mov_b32_e32 v77, v0
	v_mov_b32_e32 v78, v0
	v_mov_b32_e32 v79, v0
	v_mov_b32_e32 v84, v0
	v_mov_b32_e32 v85, v0
	v_mov_b32_e32 v86, v0
	v_mov_b32_e32 v87, v0
	v_mov_b32_e32 v92, v0
	v_mov_b32_e32 v93, v0
	v_mov_b32_e32 v94, v0
	v_mov_b32_e32 v95, v0
	v_mov_b32_e32 v100, v0
	v_mov_b32_e32 v101, v0
	v_mov_b32_e32 v102, v0
	v_mov_b32_e32 v103, v0
	v_mov_b32_e32 v108, v0
	v_mov_b32_e32 v109, v0
	v_mov_b32_e32 v110, v0
	v_mov_b32_e32 v111, v0
	v_mov_b32_e32 v116, v0
	v_mov_b32_e32 v117, v0
	v_mov_b32_e32 v118, v0
	v_mov_b32_e32 v119, v0
	v_mov_b32_e32 v72, v0
	v_mov_b32_e32 v73, v0
	v_mov_b32_e32 v74, v0
	v_mov_b32_e32 v75, v0
	v_mov_b32_e32 v80, v0
	v_mov_b32_e32 v81, v0
	v_mov_b32_e32 v82, v0
	v_mov_b32_e32 v83, v0
	v_mov_b32_e32 v88, v0
	v_mov_b32_e32 v89, v0
	v_mov_b32_e32 v90, v0
	v_mov_b32_e32 v91, v0
	v_mov_b32_e32 v96, v0
	v_mov_b32_e32 v97, v0
	v_mov_b32_e32 v98, v0
	v_mov_b32_e32 v99, v0
	v_mov_b32_e32 v104, v0
	v_mov_b32_e32 v105, v0
	v_mov_b32_e32 v106, v0
	v_mov_b32_e32 v107, v0
	v_mov_b32_e32 v112, v0
	v_mov_b32_e32 v113, v0
	v_mov_b32_e32 v114, v0
	v_mov_b32_e32 v115, v0
	v_mov_b32_e32 v120, v0
	v_mov_b32_e32 v121, v0
	v_mov_b32_e32 v122, v0
	v_mov_b32_e32 v123, v0
	v_mov_b32_e32 v124, v0
	v_mov_b32_e32 v125, v0
	v_mov_b32_e32 v126, v0
	v_mov_b32_e32 v127, v0
	.p2align 6

.LBB0_1428:
	v_mov_b32_e32 v0, 0
	s_mov_b32 s17, 0
	s_mov_b64 s[26:27], -1
	s_mov_b64 s[28:29], 0
	v_mov_b32_e32 v1, v0
	v_mov_b32_e32 v2, v0
	v_mov_b32_e32 v3, v0
	v_mov_b32_e32 v4, v0
	v_mov_b32_e32 v5, v0
	v_mov_b32_e32 v6, v0
	v_mov_b32_e32 v7, v0
	v_mov_b32_e32 v12, v0
	v_mov_b32_e32 v13, v0
	v_mov_b32_e32 v14, v0
	v_mov_b32_e32 v15, v0
	v_mov_b32_e32 v20, v0
	v_mov_b32_e32 v21, v0
	v_mov_b32_e32 v22, v0
	v_mov_b32_e32 v23, v0
	v_mov_b32_e32 v28, v0
	v_mov_b32_e32 v29, v0
	v_mov_b32_e32 v30, v0
	v_mov_b32_e32 v31, v0
	v_mov_b32_e32 v36, v0
	v_mov_b32_e32 v37, v0
	v_mov_b32_e32 v38, v0
	v_mov_b32_e32 v39, v0
	v_mov_b32_e32 v44, v0
	v_mov_b32_e32 v45, v0
	v_mov_b32_e32 v46, v0
	v_mov_b32_e32 v47, v0
	v_mov_b32_e32 v52, v0
	v_mov_b32_e32 v53, v0
	v_mov_b32_e32 v54, v0
	v_mov_b32_e32 v55, v0
	v_mov_b32_e32 v8, v0
	v_mov_b32_e32 v9, v0
	v_mov_b32_e32 v10, v0
	v_mov_b32_e32 v11, v0
	v_mov_b32_e32 v16, v0
	v_mov_b32_e32 v17, v0
	v_mov_b32_e32 v18, v0
	v_mov_b32_e32 v19, v0
	v_mov_b32_e32 v24, v0
	v_mov_b32_e32 v25, v0
	v_mov_b32_e32 v26, v0
	v_mov_b32_e32 v27, v0
	v_mov_b32_e32 v32, v0
	v_mov_b32_e32 v33, v0
	v_mov_b32_e32 v34, v0
	v_mov_b32_e32 v35, v0
	v_mov_b32_e32 v40, v0
	v_mov_b32_e32 v41, v0
	v_mov_b32_e32 v42, v0
	v_mov_b32_e32 v43, v0
	v_mov_b32_e32 v48, v0
	v_mov_b32_e32 v49, v0
	v_mov_b32_e32 v50, v0
	v_mov_b32_e32 v51, v0
	v_mov_b32_e32 v56, v0
	v_mov_b32_e32 v57, v0
	v_mov_b32_e32 v58, v0
	v_mov_b32_e32 v59, v0
	v_mov_b32_e32 v60, v0
	v_mov_b32_e32 v61, v0
	v_mov_b32_e32 v62, v0
	v_mov_b32_e32 v63, v0
	v_mov_b32_e32 v64, v0
	v_mov_b32_e32 v65, v0
	v_mov_b32_e32 v66, v0
	v_mov_b32_e32 v67, v0
	v_mov_b32_e32 v68, v0
	v_mov_b32_e32 v69, v0
	v_mov_b32_e32 v70, v0
	v_mov_b32_e32 v71, v0
	v_mov_b32_e32 v80, v0
	v_mov_b32_e32 v81, v0
	v_mov_b32_e32 v82, v0
	v_mov_b32_e32 v83, v0
	v_mov_b32_e32 v84, v0
	v_mov_b32_e32 v85, v0
	v_mov_b32_e32 v86, v0
	v_mov_b32_e32 v87, v0
	v_mov_b32_e32 v96, v0
	v_mov_b32_e32 v97, v0
	v_mov_b32_e32 v98, v0
	v_mov_b32_e32 v99, v0
	v_mov_b32_e32 v100, v0
	v_mov_b32_e32 v101, v0
	v_mov_b32_e32 v102, v0
	v_mov_b32_e32 v103, v0
	v_mov_b32_e32 v112, v0
	v_mov_b32_e32 v113, v0
	v_mov_b32_e32 v114, v0
	v_mov_b32_e32 v115, v0
	v_mov_b32_e32 v116, v0
	v_mov_b32_e32 v117, v0
	v_mov_b32_e32 v118, v0
	v_mov_b32_e32 v119, v0
	v_mov_b32_e32 v72, v0
	v_mov_b32_e32 v73, v0
	v_mov_b32_e32 v74, v0
	v_mov_b32_e32 v75, v0
	v_mov_b32_e32 v76, v0
	v_mov_b32_e32 v77, v0
	v_mov_b32_e32 v78, v0
	v_mov_b32_e32 v79, v0
	v_mov_b32_e32 v88, v0
	v_mov_b32_e32 v89, v0
	v_mov_b32_e32 v90, v0
	v_mov_b32_e32 v91, v0
	v_mov_b32_e32 v92, v0
	v_mov_b32_e32 v93, v0
	v_mov_b32_e32 v94, v0
	v_mov_b32_e32 v95, v0
	v_mov_b32_e32 v104, v0
	v_mov_b32_e32 v105, v0
	v_mov_b32_e32 v106, v0
	v_mov_b32_e32 v107, v0
	v_mov_b32_e32 v108, v0
	v_mov_b32_e32 v109, v0
	v_mov_b32_e32 v110, v0
	v_mov_b32_e32 v111, v0
	v_mov_b32_e32 v120, v0
	v_mov_b32_e32 v121, v0
	v_mov_b32_e32 v122, v0
	v_mov_b32_e32 v123, v0
	v_mov_b32_e32 v124, v0
	v_mov_b32_e32 v125, v0
	v_mov_b32_e32 v126, v0
	v_mov_b32_e32 v127, v0
	.p2align 6

.LBB0_1514:
	s_add_i32 s26, s28, 1
	s_mov_b64 s[30:31], 0
	.p2align 6

.LBB0_1613:
	s_add_i32 s14, s13, 1
	s_cmp_lg_u32 s13, 2
	s_cselect_b32 s13, s14, 0
	s_add_i32 s14, s17, 1
	s_cmp_lg_u32 s17, 2
	s_cselect_b32 s17, s14, 0
	s_add_i32 s14, s16, 1
	s_cmp_lg_u32 s16, 2
	s_cselect_b32 s16, s14, 0
	s_add_i32 s18, s18, 1
	s_addk_i32 s19, 0x2000
	s_addk_i32 s20, 0x3000
	s_cmp_eq_u32 s19, 0x200000
	s_cbranch_scc1 .LBB0_1622
	.p2align 6

.LBB0_1719:
	s_add_u32 s23, s36, 0x100
	v_mov_b32_e32 v0, 0
	s_addc_u32 s25, s37, 0
	s_mov_b32 s64, -2
	s_waitcnt lgkmcnt(0)
	v_mov_b32_e32 v1, v0
	v_mov_b32_e32 v2, v0
	v_mov_b32_e32 v3, v0
	v_mov_b32_e32 v4, v0
	v_mov_b32_e32 v5, v0
	v_mov_b32_e32 v6, v0
	v_mov_b32_e32 v7, v0
	v_mov_b32_e32 v16, v0
	v_mov_b32_e32 v17, v0
	v_mov_b32_e32 v18, v0
	v_mov_b32_e32 v19, v0
	v_mov_b32_e32 v20, v0
	v_mov_b32_e32 v21, v0
	v_mov_b32_e32 v22, v0
	v_mov_b32_e32 v23, v0
	v_mov_b32_e32 v32, v0
	v_mov_b32_e32 v33, v0
	v_mov_b32_e32 v34, v0
	v_mov_b32_e32 v35, v0
	v_mov_b32_e32 v36, v0
	v_mov_b32_e32 v37, v0
	v_mov_b32_e32 v38, v0
	v_mov_b32_e32 v39, v0
	v_mov_b32_e32 v48, v0
	v_mov_b32_e32 v49, v0
	v_mov_b32_e32 v50, v0
	v_mov_b32_e32 v51, v0
	v_mov_b32_e32 v52, v0
	v_mov_b32_e32 v53, v0
	v_mov_b32_e32 v54, v0
	v_mov_b32_e32 v55, v0
	v_mov_b32_e32 v8, v0
	v_mov_b32_e32 v9, v0
	v_mov_b32_e32 v10, v0
	v_mov_b32_e32 v11, v0
	v_mov_b32_e32 v12, v0
	v_mov_b32_e32 v13, v0
	v_mov_b32_e32 v14, v0
	v_mov_b32_e32 v15, v0
	v_mov_b32_e32 v24, v0
	v_mov_b32_e32 v25, v0
	v_mov_b32_e32 v26, v0
	v_mov_b32_e32 v27, v0
	v_mov_b32_e32 v28, v0
	v_mov_b32_e32 v29, v0
	v_mov_b32_e32 v30, v0
	v_mov_b32_e32 v31, v0
	v_mov_b32_e32 v40, v0
	v_mov_b32_e32 v41, v0
	v_mov_b32_e32 v42, v0
	v_mov_b32_e32 v43, v0
	v_mov_b32_e32 v44, v0
	v_mov_b32_e32 v45, v0
	v_mov_b32_e32 v46, v0
	v_mov_b32_e32 v47, v0
	v_mov_b32_e32 v56, v0
	v_mov_b32_e32 v57, v0
	v_mov_b32_e32 v58, v0
	v_mov_b32_e32 v59, v0
	v_mov_b32_e32 v60, v0
	v_mov_b32_e32 v61, v0
	v_mov_b32_e32 v62, v0
	v_mov_b32_e32 v63, v0
	v_mov_b32_e32 v64, v0
	v_mov_b32_e32 v65, v0
	v_mov_b32_e32 v66, v0
	v_mov_b32_e32 v67, v0
	v_mov_b32_e32 v68, v0
	v_mov_b32_e32 v69, v0
	v_mov_b32_e32 v70, v0
	v_mov_b32_e32 v71, v0
	v_mov_b32_e32 v80, v0
	v_mov_b32_e32 v81, v0
	v_mov_b32_e32 v82, v0
	v_mov_b32_e32 v83, v0
	v_mov_b32_e32 v84, v0
	v_mov_b32_e32 v85, v0
	v_mov_b32_e32 v86, v0
	v_mov_b32_e32 v87, v0
	v_mov_b32_e32 v96, v0
	v_mov_b32_e32 v97, v0
	v_mov_b32_e32 v98, v0
	v_mov_b32_e32 v99, v0
	v_mov_b32_e32 v100, v0
	v_mov_b32_e32 v101, v0
	v_mov_b32_e32 v102, v0
	v_mov_b32_e32 v103, v0
	v_mov_b32_e32 v120, v0
	v_mov_b32_e32 v121, v0
	v_mov_b32_e32 v122, v0
	v_mov_b32_e32 v123, v0
	v_mov_b32_e32 v132, v0
	v_mov_b32_e32 v133, v0
	v_mov_b32_e32 v134, v0
	v_mov_b32_e32 v135, v0
	v_mov_b32_e32 v72, v0
	v_mov_b32_e32 v73, v0
	v_mov_b32_e32 v74, v0
	v_mov_b32_e32 v75, v0
	v_mov_b32_e32 v76, v0
	v_mov_b32_e32 v77, v0
	v_mov_b32_e32 v78, v0
	v_mov_b32_e32 v79, v0
	v_mov_b32_e32 v88, v0
	v_mov_b32_e32 v89, v0
	v_mov_b32_e32 v90, v0
	v_mov_b32_e32 v91, v0
	v_mov_b32_e32 v92, v0
	v_mov_b32_e32 v93, v0
	v_mov_b32_e32 v94, v0
	v_mov_b32_e32 v95, v0
	v_mov_b32_e32 v104, v0
	v_mov_b32_e32 v105, v0
	v_mov_b32_e32 v106, v0
	v_mov_b32_e32 v107, v0
	v_mov_b32_e32 v108, v0
	v_mov_b32_e32 v109, v0
	v_mov_b32_e32 v110, v0
	v_mov_b32_e32 v111, v0
	v_mov_b32_e32 v144, v0
	v_mov_b32_e32 v145, v0
	v_mov_b32_e32 v146, v0
	v_mov_b32_e32 v147, v0
	v_mov_b32_e32 v152, v0
	v_mov_b32_e32 v153, v0
	v_mov_b32_e32 v154, v0
	v_mov_b32_e32 v155, v0
	.p2align 6

.LBB0_2032:
	s_cmp_gt_i32 s34, 23
	s_cselect_b64 s[4:5], -1, 0
	s_cmp_lt_i32 s35, 24
	s_cselect_b64 s[6:7], -1, 0
	s_or_b64 s[4:5], s[4:5], s[6:7]
	s_mov_b32 s2, 24
	s_and_b64 vcc, exec, s[4:5]
	s_cbranch_vccnz .LBB0_2328
	s_lshl_b32 s2, s2, 3
	s_add_i32 s2, s2, 0
	s_add_i32 s2, s2, 0x201c0
	v_mov_b32_e32 v0, s2
	s_waitcnt vmcnt(0) lgkmcnt(0)
	ds_read_b32 v1, v0
	ds_read_b32 v0, v0 offset:4
	s_and_b32 s42, s33, 0xffffffc0
	v_mbcnt_lo_u32_b32 v2, -1, 0
	v_mbcnt_hi_u32_b32 v2, -1, v2
	s_waitcnt lgkmcnt(1)
	v_readfirstlane_b32 s2, v1
	s_waitcnt lgkmcnt(0)
	v_readfirstlane_b32 s3, v0
	v_add_u32_e32 v0, s42, v2
	v_cmp_gt_i32_e32 vcc, 64, v0
	s_and_saveexec_b64 s[4:5], vcc
	s_cbranch_execz .LBB0_2049
	v_lshlrev_b32_e32 v2, 5, v0
	v_ashrrev_i32_e32 v3, 31, v2
	v_lshl_add_u64 v[2:3], v[2:3], 2, s[2:3]
	v_add_co_u32_e32 v2, vcc, 0xa000, v2
	v_lshlrev_b32_e32 v9, 2, v0
	s_nop 0
	v_addc_co_u32_e32 v3, vcc, 0, v3, vcc
	global_load_dword v8, v[2:3], off sc1
	v_add_u32_e32 v1, -4, v9
	v_cmp_lt_i32_e32 vcc, 0, v0
	v_add_u32_e32 v4, -8, v9
	v_add_u32_e32 v5, -16, v9
	v_subrev_u32_e32 v6, 32, v9
	v_subrev_u32_e32 v7, 64, v9
	v_add_u32_e32 v10, 0xffffff80, v9
	v_add_u32_e32 v9, 0, v9
	v_add_u32_e32 v9, 0x20a00, v9
	s_waitcnt vmcnt(0)
	v_add_u32_e32 v2, 0xff, v8
	v_ashrrev_i32_e32 v2, 8, v2
	ds_bpermute_b32 v1, v1, v2
	ds_write_b32 v9, v8
	s_waitcnt lgkmcnt(1)
	v_cndmask_b32_e32 v3, 0, v1, vcc
	v_add_u32_e32 v1, v3, v2
	ds_bpermute_b32 v4, v4, v1
	v_cmp_lt_i32_e32 vcc, 1, v0
	s_waitcnt lgkmcnt(0)
	s_nop 0
	v_cndmask_b32_e32 v4, 0, v4, vcc
	v_add_u32_e32 v1, v4, v1
	ds_bpermute_b32 v5, v5, v1
	v_cmp_lt_i32_e32 vcc, 3, v0
	s_waitcnt lgkmcnt(0)
	s_nop 0
	v_cndmask_b32_e32 v5, 0, v5, vcc
	v_add_u32_e32 v1, v5, v1
	ds_bpermute_b32 v6, v6, v1
	v_cmp_lt_i32_e32 vcc, 7, v0
	s_waitcnt lgkmcnt(0)
	s_nop 0
	v_cndmask_b32_e32 v6, 0, v6, vcc
	v_add_u32_e32 v1, v6, v1
	ds_bpermute_b32 v7, v7, v1
	v_cmp_lt_i32_e32 vcc, 15, v0
	s_waitcnt lgkmcnt(0)
	s_nop 0
	v_cndmask_b32_e32 v7, 0, v7, vcc
	v_add_u32_e32 v1, v7, v1
	ds_bpermute_b32 v10, v10, v1
	v_cmp_lt_i32_e32 vcc, 31, v0
	s_waitcnt lgkmcnt(0)
	s_nop 0
	v_cndmask_b32_e32 v9, 0, v10, vcc
	v_cmp_eq_u32_e32 vcc, 63, v0
	s_and_saveexec_b64 s[6:7], vcc
	s_add_i32 s8, 0, 0x20b00
	v_add_u32_e32 v1, v9, v1
	v_mov_b32_e32 v8, s8
	ds_write_b32 v8, v1
	s_or_b64 exec, exec, s[6:7]
	v_cmp_lt_i32_e32 vcc, 0, v2
	s_and_b64 exec, exec, vcc
	s_cbranch_execz .LBB0_2049
	v_lshlrev_b32_e32 v8, 16, v0
	v_cmp_ne_u32_e32 vcc, 1, v2
	s_mov_b64 s[8:9], -1
	v_mov_b32_e32 v0, 0
	s_and_saveexec_b64 s[6:7], vcc
	s_cbranch_execz .LBB0_2046
	v_add_u32_e32 v0, -2, v2
	v_lshrrev_b32_e32 v1, 1, v0
	v_cmp_lt_u32_e32 vcc, 13, v0
	v_mov_b32_e32 v0, 0
	v_add_u32_e32 v10, 1, v1
	s_mov_b32 s16, 0
	v_mov_b32_e32 v1, 1
	v_mov_b32_e32 v13, v0
	s_and_saveexec_b64 s[8:9], vcc
	s_cbranch_execz .LBB0_2042
	v_add_u32_e32 v0, v3, v4
	v_add3_u32 v0, v0, v5, v6
	v_add3_u32 v0, v0, v7, v9
	v_lshl_add_u32 v0, v0, 2, 0
	v_and_b32_e32 v11, -8, v10
	v_add_u32_e32 v12, 0x20400, v0
	s_mov_b32 s15, 1
	s_mov_b64 s[12:13], 0
	s_mov_b32 s14, 0
	.p2align 6

.LBB0_2328:
	s_cmp_gt_i32 s34, 24
	s_cselect_b64 s[2:3], -1, 0
	s_cmp_lt_i32 s35, 25
	s_cselect_b64 s[4:5], -1, 0
	s_or_b64 s[2:3], s[2:3], s[4:5]
	s_and_b64 vcc, exec, s[2:3]
	s_cbranch_vccnz .LBB0_2447
	s_mov_b32 s2, 24
	s_lshl_b32 s2, s2, 3
	s_add_i32 s2, s2, 0
	s_add_i32 s2, s2, 0x201c0
	v_mov_b32_e32 v0, s2
	s_waitcnt vmcnt(0) lgkmcnt(0)
	ds_read_b32 v1, v0
	ds_read_b32 v0, v0 offset:4
	s_and_b32 s40, s33, 0xffffffc0
	v_mbcnt_lo_u32_b32 v2, -1, 0
	v_mbcnt_hi_u32_b32 v2, -1, v2
	s_waitcnt lgkmcnt(1)
	v_readfirstlane_b32 s18, v1
	s_waitcnt lgkmcnt(0)
	v_readfirstlane_b32 s19, v0
	v_add_u32_e32 v0, s40, v2
	v_cmp_gt_i32_e32 vcc, 64, v0
	s_and_saveexec_b64 s[2:3], vcc
	s_cbranch_execz .LBB0_2345
	v_lshlrev_b32_e32 v2, 5, v0
	v_ashrrev_i32_e32 v3, 31, v2
	v_lshl_add_u64 v[2:3], v[2:3], 2, s[18:19]
	v_add_co_u32_e32 v2, vcc, 0xa000, v2
	v_lshlrev_b32_e32 v9, 2, v0
	s_nop 0
	v_addc_co_u32_e32 v3, vcc, 0, v3, vcc
	global_load_dword v8, v[2:3], off sc1
	v_add_u32_e32 v1, -4, v9
	v_cmp_lt_i32_e32 vcc, 0, v0
	v_add_u32_e32 v4, -8, v9
	v_add_u32_e32 v5, -16, v9
	v_subrev_u32_e32 v6, 32, v9
	v_subrev_u32_e32 v7, 64, v9
	v_add_u32_e32 v10, 0xffffff80, v9
	v_add_u32_e32 v9, 0, v9
	v_add_u32_e32 v9, 0x20a00, v9
	s_waitcnt vmcnt(0)
	v_add_u32_e32 v2, 0xff, v8
	v_ashrrev_i32_e32 v2, 8, v2
	ds_bpermute_b32 v1, v1, v2
	ds_write_b32 v9, v8
	s_waitcnt lgkmcnt(1)
	v_cndmask_b32_e32 v3, 0, v1, vcc
	v_add_u32_e32 v1, v3, v2
	ds_bpermute_b32 v4, v4, v1
	v_cmp_lt_i32_e32 vcc, 1, v0
	s_waitcnt lgkmcnt(0)
	s_nop 0
	v_cndmask_b32_e32 v4, 0, v4, vcc
	v_add_u32_e32 v1, v4, v1
	ds_bpermute_b32 v5, v5, v1
	v_cmp_lt_i32_e32 vcc, 3, v0
	s_waitcnt lgkmcnt(0)
	s_nop 0
	v_cndmask_b32_e32 v5, 0, v5, vcc
	v_add_u32_e32 v1, v5, v1
	ds_bpermute_b32 v6, v6, v1
	v_cmp_lt_i32_e32 vcc, 7, v0
	s_waitcnt lgkmcnt(0)
	s_nop 0
	v_cndmask_b32_e32 v6, 0, v6, vcc
	v_add_u32_e32 v1, v6, v1
	ds_bpermute_b32 v7, v7, v1
	v_cmp_lt_i32_e32 vcc, 15, v0
	s_waitcnt lgkmcnt(0)
	s_nop 0
	v_cndmask_b32_e32 v7, 0, v7, vcc
	v_add_u32_e32 v1, v7, v1
	ds_bpermute_b32 v10, v10, v1
	v_cmp_lt_i32_e32 vcc, 31, v0
	s_waitcnt lgkmcnt(0)
	s_nop 0
	v_cndmask_b32_e32 v9, 0, v10, vcc
	v_cmp_eq_u32_e32 vcc, 63, v0
	s_and_saveexec_b64 s[4:5], vcc
	s_add_i32 s6, 0, 0x20b00
	v_add_u32_e32 v1, v9, v1
	v_mov_b32_e32 v8, s6
	ds_write_b32 v8, v1
	s_or_b64 exec, exec, s[4:5]
	v_cmp_lt_i32_e32 vcc, 0, v2
	s_and_b64 exec, exec, vcc
	s_cbranch_execz .LBB0_2345
	v_lshlrev_b32_e32 v8, 16, v0
	v_cmp_ne_u32_e32 vcc, 1, v2
	s_mov_b64 s[6:7], -1
	v_mov_b32_e32 v0, 0
	s_and_saveexec_b64 s[4:5], vcc
	s_cbranch_execz .LBB0_2342
	v_add_u32_e32 v0, -2, v2
	v_lshrrev_b32_e32 v1, 1, v0
	v_cmp_lt_u32_e32 vcc, 13, v0
	v_mov_b32_e32 v0, 0
	v_add_u32_e32 v10, 1, v1
	s_mov_b32 s14, 0
	v_mov_b32_e32 v1, 1
	v_mov_b32_e32 v13, v0
	s_and_saveexec_b64 s[6:7], vcc
	s_cbranch_execz .LBB0_2338
	v_add_u32_e32 v0, v3, v4
	v_add3_u32 v0, v0, v5, v6
	v_add3_u32 v0, v0, v7, v9
	v_lshl_add_u32 v0, v0, 2, 0
	v_and_b32_e32 v11, -8, v10
	v_add_u32_e32 v12, 0x20400, v0
	s_mov_b32 s13, 1
	s_mov_b64 s[8:9], 0
	s_mov_b32 s12, 0
	.p2align 6

.LBB0_2613:
	s_or_b64 exec, exec, s[22:23]
	v_lshlrev_b32_e32 v46, 2, v22
	global_load_dwordx4 v[22:25], v46, s[12:13]
	global_load_dwordx4 v[26:29], v46, s[18:19]
	global_load_dwordx4 v[30:33], v46, s[12:13] offset:16
	global_load_dwordx4 v[34:37], v46, s[18:19] offset:16
	global_load_dwordx4 v[38:41], v46, s[16:17]
	global_load_dwordx4 v[42:45], v46, s[16:17] offset:16
	s_waitcnt vmcnt(6)
	v_lshlrev_b32_e32 v52, 16, v4
	v_lshlrev_b32_e32 v53, 16, v0
	v_lshlrev_b32_e32 v47, 16, v12
	v_lshlrev_b32_e32 v46, 16, v8
	v_and_b32_e32 v54, 0xffff0000, v4
	v_and_b32_e32 v55, 0xffff0000, v0
	v_and_b32_e32 v49, 0xffff0000, v12
	v_and_b32_e32 v48, 0xffff0000, v8
	v_lshlrev_b32_e32 v56, 16, v5
	v_lshlrev_b32_e32 v57, 16, v1
	v_lshlrev_b32_e32 v50, 16, v9
	v_lshlrev_b32_e32 v51, 16, v13
	v_and_b32_e32 v58, 0xffff0000, v5
	v_and_b32_e32 v59, 0xffff0000, v1
	v_and_b32_e32 v1, 0xffff0000, v13
	v_and_b32_e32 v0, 0xffff0000, v9
	v_lshlrev_b32_e32 v60, 16, v6
	v_lshlrev_b32_e32 v61, 16, v2
	v_lshlrev_b32_e32 v5, 16, v14
	v_lshlrev_b32_e32 v4, 16, v10
	v_and_b32_e32 v62, 0xffff0000, v6
	v_and_b32_e32 v63, 0xffff0000, v2
	v_and_b32_e32 v9, 0xffff0000, v14
	v_and_b32_e32 v8, 0xffff0000, v10
	v_lshlrev_b32_e32 v64, 16, v7
	v_lshlrev_b32_e32 v65, 16, v3
	v_lshlrev_b32_e32 v12, 16, v11
	v_lshlrev_b32_e32 v13, 16, v15
	v_and_b32_e32 v66, 0xffff0000, v7
	v_and_b32_e32 v67, 0xffff0000, v3
	v_and_b32_e32 v3, 0xffff0000, v15
	v_and_b32_e32 v2, 0xffff0000, v11
	v_lshlrev_b64 v[18:19], 10, v[18:19]
	v_add_u32_e32 v20, s26, v20
	v_cmp_lt_i32_e32 vcc, s29, v20
	s_or_b64 s[20:21], vcc, s[20:21]
	v_add_u32_e32 v21, s27, v21
	s_waitcnt vmcnt(5)
	v_mov_b32_e32 v6, v22
	s_waitcnt vmcnt(4)
	v_mov_b32_e32 v7, v26
	v_mov_b32_e32 v26, v23
	v_mov_b32_e32 v11, v28
	v_mov_b32_e32 v28, v25
	s_waitcnt vmcnt(3)
	v_mov_b32_e32 v14, v30
	s_waitcnt vmcnt(2)
	v_mov_b32_e32 v15, v34
	v_mov_b32_e32 v34, v31
	v_mov_b32_e32 v22, v32
	v_mov_b32_e32 v23, v36
	v_mov_b32_e32 v10, v24
	v_mov_b32_e32 v36, v33
	v_pk_mul_f32 v[6:7], v[6:7], v[46:47]
	v_pk_mul_f32 v[0:1], v[28:29], v[0:1]
	v_pk_mul_f32 v[4:5], v[14:15], v[4:5]
	v_pk_mul_f32 v[8:9], v[34:35], v[8:9]
	v_pk_mul_f32 v[12:13], v[22:23], v[12:13]
	v_pk_mul_f32 v[24:25], v[26:27], v[48:49]
	v_pk_mul_f32 v[10:11], v[10:11], v[50:51]
	v_pk_mul_f32 v[2:3], v[36:37], v[2:3]
	s_waitcnt vmcnt(1)
	v_fma_f32 v6, v38, v53, v6
	v_fma_f32 v0, v41, v59, v0
	s_waitcnt vmcnt(0)
	v_fma_f32 v4, v42, v61, v4
	v_fma_f32 v8, v43, v63, v8
	v_fma_f32 v12, v44, v65, v12
	v_fma_f32 v14, v39, v55, v24
	v_fma_f32 v10, v40, v57, v10
	v_fma_f32 v2, v45, v67, v2
	v_add_f32_e32 v6, v6, v7
	v_add_f32_e32 v0, v0, v1
	v_add_f32_e32 v1, v4, v5
	v_add_f32_e32 v4, v8, v9
	v_add_f32_e32 v5, v12, v13
	v_add_f32_e32 v7, v14, v25
	v_add_f32_e32 v10, v10, v11
	v_add_f32_e32 v2, v2, v3
	v_mul_f32_e32 v3, v6, v52
	v_mul_f32_e32 v4, v4, v62
	v_mul_f32_e32 v5, v5, v64
	v_mul_f32_e32 v6, v7, v54
	v_mul_f32_e32 v7, v10, v56
	v_mul_f32_e32 v8, v0, v58
	v_mul_f32_e32 v9, v1, v60
	v_mul_f32_e32 v10, v2, v66
	v_cvt_pk_bf16_f32 v0, v3, v6
	v_cvt_pk_bf16_f32 v2, v9, v4
	v_cvt_pk_bf16_f32 v3, v5, v10
	v_lshl_add_u64 v[4:5], v[18:19], 1, s[14:15]
	v_lshl_add_u64 v[4:5], v[4:5], 0, v[16:17]
	v_cvt_pk_bf16_f32 v1, v7, v8
	global_store_dwordx4 v[4:5], v[0:3], off
	s_andn2_b64 exec, exec, s[20:21]
	s_cbranch_execz .LBB0_2618
	.p2align 6

.LBB0_3016:
	s_cmp_gt_i32 s34, 35
	s_cselect_b64 s[2:3], -1, 0
	s_cmp_lt_i32 s35, 36
	s_cselect_b64 s[4:5], -1, 0
	s_or_b64 s[2:3], s[2:3], s[4:5]
	s_and_b64 vcc, exec, s[2:3]
	s_cbranch_vccnz .LBB0_3312
	s_mov_b32 s2, 24
	s_lshl_b32 s2, s2, 3
	s_add_i32 s2, s2, 0
	s_add_i32 s2, s2, 0x201c0
	v_mov_b32_e32 v0, s2
	s_waitcnt vmcnt(0) lgkmcnt(0)
	ds_read_b32 v1, v0
	ds_read_b32 v0, v0 offset:4
	s_and_b32 s42, s33, 0xffffffc0
	v_mbcnt_lo_u32_b32 v2, -1, 0
	v_mbcnt_hi_u32_b32 v2, -1, v2
	s_waitcnt lgkmcnt(1)
	v_readfirstlane_b32 s2, v1
	s_waitcnt lgkmcnt(0)
	v_readfirstlane_b32 s3, v0
	v_add_u32_e32 v0, s42, v2
	v_cmp_gt_i32_e32 vcc, 64, v0
	s_and_saveexec_b64 s[4:5], vcc
	s_cbranch_execz .LBB0_3033
	v_lshlrev_b32_e32 v2, 5, v0
	v_ashrrev_i32_e32 v3, 31, v2
	v_lshl_add_u64 v[2:3], v[2:3], 2, s[2:3]
	v_add_co_u32_e32 v2, vcc, 0xc000, v2
	v_lshlrev_b32_e32 v9, 2, v0
	s_nop 0
	v_addc_co_u32_e32 v3, vcc, 0, v3, vcc
	global_load_dword v8, v[2:3], off sc1
	v_add_u32_e32 v1, -4, v9
	v_cmp_lt_i32_e32 vcc, 0, v0
	v_add_u32_e32 v4, -8, v9
	v_add_u32_e32 v5, -16, v9
	v_subrev_u32_e32 v6, 32, v9
	v_subrev_u32_e32 v7, 64, v9
	v_add_u32_e32 v10, 0xffffff80, v9
	v_add_u32_e32 v9, 0, v9
	v_add_u32_e32 v9, 0x20a00, v9
	s_waitcnt vmcnt(0)
	v_add_u32_e32 v2, 0xff, v8
	v_ashrrev_i32_e32 v2, 8, v2
	ds_bpermute_b32 v1, v1, v2
	ds_write_b32 v9, v8
	s_waitcnt lgkmcnt(1)
	v_cndmask_b32_e32 v3, 0, v1, vcc
	v_add_u32_e32 v1, v3, v2
	ds_bpermute_b32 v4, v4, v1
	v_cmp_lt_i32_e32 vcc, 1, v0
	s_waitcnt lgkmcnt(0)
	s_nop 0
	v_cndmask_b32_e32 v4, 0, v4, vcc
	v_add_u32_e32 v1, v4, v1
	ds_bpermute_b32 v5, v5, v1
	v_cmp_lt_i32_e32 vcc, 3, v0
	s_waitcnt lgkmcnt(0)
	s_nop 0
	v_cndmask_b32_e32 v5, 0, v5, vcc
	v_add_u32_e32 v1, v5, v1
	ds_bpermute_b32 v6, v6, v1
	v_cmp_lt_i32_e32 vcc, 7, v0
	s_waitcnt lgkmcnt(0)
	s_nop 0
	v_cndmask_b32_e32 v6, 0, v6, vcc
	v_add_u32_e32 v1, v6, v1
	ds_bpermute_b32 v7, v7, v1
	v_cmp_lt_i32_e32 vcc, 15, v0
	s_waitcnt lgkmcnt(0)
	s_nop 0
	v_cndmask_b32_e32 v7, 0, v7, vcc
	v_add_u32_e32 v1, v7, v1
	ds_bpermute_b32 v10, v10, v1
	v_cmp_lt_i32_e32 vcc, 31, v0
	s_waitcnt lgkmcnt(0)
	s_nop 0
	v_cndmask_b32_e32 v9, 0, v10, vcc
	v_cmp_eq_u32_e32 vcc, 63, v0
	s_and_saveexec_b64 s[6:7], vcc
	s_add_i32 s8, 0, 0x20b00
	v_add_u32_e32 v1, v9, v1
	v_mov_b32_e32 v8, s8
	ds_write_b32 v8, v1
	s_or_b64 exec, exec, s[6:7]
	v_cmp_lt_i32_e32 vcc, 0, v2
	s_and_b64 exec, exec, vcc
	s_cbranch_execz .LBB0_3033
	v_lshlrev_b32_e32 v8, 16, v0
	v_cmp_ne_u32_e32 vcc, 1, v2
	s_mov_b64 s[8:9], -1
	v_mov_b32_e32 v0, 0
	s_and_saveexec_b64 s[6:7], vcc
	s_cbranch_execz .LBB0_3030
	v_add_u32_e32 v0, -2, v2
	v_lshrrev_b32_e32 v1, 1, v0
	v_cmp_lt_u32_e32 vcc, 13, v0
	v_mov_b32_e32 v0, 0
	v_add_u32_e32 v10, 1, v1
	s_mov_b32 s16, 0
	v_mov_b32_e32 v1, 1
	v_mov_b32_e32 v13, v0
	s_and_saveexec_b64 s[8:9], vcc
	s_cbranch_execz .LBB0_3026
	v_add_u32_e32 v0, v3, v4
	v_add3_u32 v0, v0, v5, v6
	v_add3_u32 v0, v0, v7, v9
	v_lshl_add_u32 v0, v0, 2, 0
	v_and_b32_e32 v11, -8, v10
	v_add_u32_e32 v12, 0x20400, v0
	s_mov_b32 s15, 1
	s_mov_b64 s[12:13], 0
	s_mov_b32 s14, 0
	.p2align 6

.LBB0_3212:
	ds_read2_b32 v[214:215], v146 offset1:32
	s_add_i32 s44, s44, s29
	s_add_i32 s28, s28, s29
	s_add_i32 s54, s54, s29
	s_add_i32 s55, s55, s56
	s_waitcnt vmcnt(0) lgkmcnt(0)
	v_mul_f32_e32 v77, v68, v214
	ds_read_b32 v209, v147
	ds_read_b32 v211, v148
	ds_read_b32 v212, v149
	ds_read_b32 v213, v150
	ds_read_b32 v214, v151
	ds_read_b32 v216, v152
	ds_read_b32 v217, v153
	ds_read_b32 v218, v154
	s_waitcnt lgkmcnt(7)
	v_mul_f32_e32 v209, v69, v209
	v_cvt_pk_bf16_f32 v210, v77, v209
	s_waitcnt lgkmcnt(6)
	v_mul_f32_e32 v77, v70, v211
	s_waitcnt lgkmcnt(5)
	v_mul_f32_e32 v209, v71, v212
	v_cvt_pk_bf16_f32 v211, v77, v209
	s_waitcnt lgkmcnt(4)
	v_mul_f32_e32 v77, v64, v213
	s_waitcnt lgkmcnt(3)
	v_mul_f32_e32 v209, v65, v214
	v_cvt_pk_bf16_f32 v212, v77, v209
	s_waitcnt lgkmcnt(2)
	v_mul_f32_e32 v77, v66, v216
	s_waitcnt lgkmcnt(1)
	v_mul_f32_e32 v209, v67, v217
	v_cvt_pk_bf16_f32 v213, v77, v209
	v_add_u32_e32 v77, s27, v138
	v_mad_i64_i32 v[216:217], s[6:7], s26, v77, 0
	v_lshl_add_u64 v[216:217], v[216:217], 1, s[2:3]
	s_lshl_b64 s[6:7], s[8:9], 1
	v_lshl_add_u64 v[216:217], v[216:217], 0, s[6:7]
	v_lshl_add_u64 v[216:217], v[216:217], 0, v[72:73]
	global_store_dwordx4 v[216:217], v[210:213], off
	s_waitcnt lgkmcnt(0)
	v_mul_f32_e32 v77, v68, v218
	ds_read_b32 v209, v155
	ds_read_b32 v211, v156
	ds_read_b32 v212, v157
	ds_read_b32 v213, v158
	ds_read_b32 v214, v159
	ds_read_b32 v216, v160
	ds_read_b32 v217, v161
	ds_read_b32 v218, v162
	s_waitcnt lgkmcnt(7)
	v_mul_f32_e32 v209, v69, v209
	v_cvt_pk_bf16_f32 v210, v77, v209
	s_waitcnt lgkmcnt(6)
	v_mul_f32_e32 v77, v70, v211
	s_waitcnt lgkmcnt(5)
	v_mul_f32_e32 v209, v71, v212
	v_cvt_pk_bf16_f32 v211, v77, v209
	s_waitcnt lgkmcnt(4)
	v_mul_f32_e32 v77, v64, v213
	s_waitcnt lgkmcnt(3)
	v_mul_f32_e32 v209, v65, v214
	v_cvt_pk_bf16_f32 v212, v77, v209
	s_waitcnt lgkmcnt(2)
	v_mul_f32_e32 v77, v66, v216
	s_waitcnt lgkmcnt(1)
	v_mul_f32_e32 v209, v67, v217
	v_cvt_pk_bf16_f32 v213, v77, v209
	v_add_u32_e32 v77, s27, v139
	v_mad_i64_i32 v[216:217], s[8:9], s26, v77, 0
	v_lshl_add_u64 v[216:217], v[216:217], 1, s[2:3]
	v_lshl_add_u64 v[216:217], v[216:217], 0, s[6:7]
	v_lshl_add_u64 v[216:217], v[216:217], 0, v[72:73]
	global_store_dwordx4 v[216:217], v[210:213], off
	s_waitcnt lgkmcnt(0)
	v_mul_f32_e32 v77, v68, v218
	ds_read_b32 v209, v163
	ds_read_b32 v211, v164
	ds_read_b32 v212, v165
	ds_read_b32 v213, v166
	ds_read_b32 v214, v167
	ds_read_b32 v216, v168
	ds_read_b32 v217, v169
	ds_read_b32 v218, v170
	s_waitcnt lgkmcnt(7)
	v_mul_f32_e32 v209, v69, v209
	v_cvt_pk_bf16_f32 v210, v77, v209
	s_waitcnt lgkmcnt(6)
	v_mul_f32_e32 v77, v70, v211
	s_waitcnt lgkmcnt(5)
	v_mul_f32_e32 v209, v71, v212
	v_cvt_pk_bf16_f32 v211, v77, v209
	s_waitcnt lgkmcnt(4)
	v_mul_f32_e32 v77, v64, v213
	s_waitcnt lgkmcnt(3)
	v_mul_f32_e32 v209, v65, v214
	v_cvt_pk_bf16_f32 v212, v77, v209
	s_waitcnt lgkmcnt(2)
	v_mul_f32_e32 v77, v66, v216
	s_waitcnt lgkmcnt(1)
	v_mul_f32_e32 v209, v67, v217
	v_cvt_pk_bf16_f32 v213, v77, v209
	v_add_u32_e32 v77, s27, v140
	v_mad_i64_i32 v[216:217], s[8:9], s26, v77, 0
	v_lshl_add_u64 v[216:217], v[216:217], 1, s[2:3]
	v_lshl_add_u64 v[216:217], v[216:217], 0, s[6:7]
	v_lshl_add_u64 v[216:217], v[216:217], 0, v[72:73]
	global_store_dwordx4 v[216:217], v[210:213], off
	s_waitcnt lgkmcnt(0)
	v_mul_f32_e32 v77, v68, v218
	ds_read_b32 v209, v171
	ds_read_b32 v211, v172
	ds_read_b32 v212, v173
	ds_read_b32 v213, v174
	ds_read_b32 v214, v175
	ds_read_b32 v216, v176
	ds_read_b32 v217, v177
	ds_read_b32 v218, v178
	s_waitcnt lgkmcnt(7)
	v_mul_f32_e32 v209, v69, v209
	v_cvt_pk_bf16_f32 v210, v77, v209
	s_waitcnt lgkmcnt(6)
	v_mul_f32_e32 v77, v70, v211
	s_waitcnt lgkmcnt(5)
	v_mul_f32_e32 v209, v71, v212
	v_cvt_pk_bf16_f32 v211, v77, v209
	s_waitcnt lgkmcnt(4)
	v_mul_f32_e32 v77, v64, v213
	s_waitcnt lgkmcnt(3)
	v_mul_f32_e32 v209, v65, v214
	v_cvt_pk_bf16_f32 v212, v77, v209
	s_waitcnt lgkmcnt(2)
	v_mul_f32_e32 v77, v66, v216
	s_waitcnt lgkmcnt(1)
	v_mul_f32_e32 v209, v67, v217
	v_cvt_pk_bf16_f32 v213, v77, v209
	v_add_u32_e32 v77, s27, v141
	v_mad_i64_i32 v[216:217], s[8:9], s26, v77, 0
	v_lshl_add_u64 v[216:217], v[216:217], 1, s[2:3]
	v_lshl_add_u64 v[216:217], v[216:217], 0, s[6:7]
	v_lshl_add_u64 v[216:217], v[216:217], 0, v[72:73]
	global_store_dwordx4 v[216:217], v[210:213], off
	v_mul_f32_e32 v77, v68, v215
	s_waitcnt lgkmcnt(0)
	v_mul_f32_e32 v209, v69, v218
	v_cvt_pk_bf16_f32 v210, v77, v209
	ds_read_b32 v77, v179
	ds_read_b32 v209, v180
	ds_read_b32 v212, v181
	ds_read_b32 v213, v182
	ds_read_b32 v214, v183
	ds_read_b32 v215, v184
	ds_read_b32 v216, v185
	ds_read_b32 v217, v186
	s_waitcnt lgkmcnt(7)
	v_mul_f32_e32 v77, v70, v77
	s_waitcnt lgkmcnt(6)
	v_mul_f32_e32 v209, v71, v209
	v_cvt_pk_bf16_f32 v211, v77, v209
	s_waitcnt lgkmcnt(5)
	v_mul_f32_e32 v77, v64, v212
	s_waitcnt lgkmcnt(4)
	v_mul_f32_e32 v209, v65, v213
	v_cvt_pk_bf16_f32 v212, v77, v209
	s_waitcnt lgkmcnt(3)
	v_mul_f32_e32 v77, v66, v214
	s_waitcnt lgkmcnt(2)
	v_mul_f32_e32 v209, v67, v215
	v_cvt_pk_bf16_f32 v213, v77, v209
	v_add_u32_e32 v77, s27, v142
	v_mad_i64_i32 v[214:215], s[8:9], s26, v77, 0
	v_lshl_add_u64 v[214:215], v[214:215], 1, s[2:3]
	v_lshl_add_u64 v[214:215], v[214:215], 0, s[6:7]
	v_lshl_add_u64 v[214:215], v[214:215], 0, v[72:73]
	global_store_dwordx4 v[214:215], v[210:213], off
	s_waitcnt lgkmcnt(1)
	v_mul_f32_e32 v77, v68, v216
	s_waitcnt lgkmcnt(0)
	v_mul_f32_e32 v209, v69, v217
	v_cvt_pk_bf16_f32 v210, v77, v209
	ds_read_b32 v77, v187
	ds_read_b32 v209, v188
	ds_read_b32 v212, v189
	ds_read_b32 v213, v190
	ds_read_b32 v214, v191
	ds_read_b32 v215, v192
	ds_read_b32 v216, v193
	ds_read_b32 v217, v194
	s_waitcnt lgkmcnt(7)
	v_mul_f32_e32 v77, v70, v77
	s_waitcnt lgkmcnt(6)
	v_mul_f32_e32 v209, v71, v209
	v_cvt_pk_bf16_f32 v211, v77, v209
	s_waitcnt lgkmcnt(5)
	v_mul_f32_e32 v77, v64, v212
	s_waitcnt lgkmcnt(4)
	v_mul_f32_e32 v209, v65, v213
	v_cvt_pk_bf16_f32 v212, v77, v209
	s_waitcnt lgkmcnt(3)
	v_mul_f32_e32 v77, v66, v214
	s_waitcnt lgkmcnt(2)
	v_mul_f32_e32 v209, v67, v215
	v_cvt_pk_bf16_f32 v213, v77, v209
	v_add_u32_e32 v77, s27, v143
	v_mad_i64_i32 v[214:215], s[8:9], s26, v77, 0
	v_lshl_add_u64 v[214:215], v[214:215], 1, s[2:3]
	v_lshl_add_u64 v[214:215], v[214:215], 0, s[6:7]
	v_lshl_add_u64 v[214:215], v[214:215], 0, v[72:73]
	global_store_dwordx4 v[214:215], v[210:213], off
	s_waitcnt lgkmcnt(1)
	v_mul_f32_e32 v77, v68, v216
	s_waitcnt lgkmcnt(0)
	v_mul_f32_e32 v209, v69, v217
	v_cvt_pk_bf16_f32 v210, v77, v209
	ds_read_b32 v77, v195
	ds_read_b32 v209, v196
	ds_read_b32 v212, v197
	ds_read_b32 v213, v198
	ds_read_b32 v214, v199
	ds_read_b32 v215, v200
	ds_read_b32 v216, v201
	ds_read_b32 v217, v202
	s_waitcnt lgkmcnt(7)
	v_mul_f32_e32 v77, v70, v77
	s_waitcnt lgkmcnt(6)
	v_mul_f32_e32 v209, v71, v209
	v_cvt_pk_bf16_f32 v211, v77, v209
	s_waitcnt lgkmcnt(5)
	v_mul_f32_e32 v77, v64, v212
	s_waitcnt lgkmcnt(4)
	v_mul_f32_e32 v209, v65, v213
	v_cvt_pk_bf16_f32 v212, v77, v209
	s_waitcnt lgkmcnt(3)
	v_mul_f32_e32 v77, v66, v214
	s_waitcnt lgkmcnt(2)
	v_mul_f32_e32 v209, v67, v215
	v_cvt_pk_bf16_f32 v213, v77, v209
	v_add_u32_e32 v77, s27, v144
	v_mad_i64_i32 v[214:215], s[8:9], s26, v77, 0
	v_lshl_add_u64 v[214:215], v[214:215], 1, s[2:3]
	v_lshl_add_u64 v[214:215], v[214:215], 0, s[6:7]
	v_lshl_add_u64 v[214:215], v[214:215], 0, v[72:73]
	global_store_dwordx4 v[214:215], v[210:213], off
	ds_read_b32 v77, v203
	ds_read_b32 v209, v204
	ds_read_b32 v210, v205
	ds_read_b32 v211, v206
	ds_read_b32 v212, v207
	ds_read_b32 v213, v208
	s_waitcnt lgkmcnt(7)
	v_mul_f32_e32 v68, v68, v216
	s_waitcnt lgkmcnt(6)
	v_mul_f32_e32 v69, v69, v217
	v_cvt_pk_bf16_f32 v68, v68, v69
	s_waitcnt lgkmcnt(5)
	v_mul_f32_e32 v69, v70, v77
	s_waitcnt lgkmcnt(4)
	v_mul_f32_e32 v70, v71, v209
	s_waitcnt lgkmcnt(3)
	v_mul_f32_e32 v64, v64, v210
	v_cvt_pk_bf16_f32 v69, v69, v70
	s_waitcnt lgkmcnt(2)
	v_mul_f32_e32 v65, v65, v211
	v_cvt_pk_bf16_f32 v70, v64, v65
	s_waitcnt lgkmcnt(1)
	v_mul_f32_e32 v64, v66, v212
	s_waitcnt lgkmcnt(0)
	v_mul_f32_e32 v65, v67, v213
	v_cvt_pk_bf16_f32 v71, v64, v65
	v_add_u32_e32 v64, s27, v145
	v_mad_i64_i32 v[64:65], s[8:9], s26, v64, 0
	v_lshl_add_u64 v[64:65], v[64:65], 1, s[2:3]
	v_lshl_add_u64 v[64:65], v[64:65], 0, s[6:7]
	v_lshl_add_u64 v[64:65], v[64:65], 0, v[72:73]
	global_store_dwordx4 v[64:65], v[68:71], off
	s_waitcnt lgkmcnt(0)
	s_add_i32 s2, s53, s44
	s_cmpk_gt_i32 s2, 0x13ff
	s_mov_b32 s27, s24
	s_mov_b64 s[2:3], s[12:13]
	s_mov_b64 s[6:7], s[14:15]
	s_mov_b32 s26, s57
	s_mov_b32 s8, s18
	s_cbranch_scc1 .LBB0_3246
	.p2align 6

.LBB0_3312:
	s_cmp_gt_i32 s34, 36
	s_cselect_b64 s[2:3], -1, 0
	s_cmp_lt_i32 s35, 37
	s_cselect_b64 s[4:5], -1, 0
	s_or_b64 s[2:3], s[2:3], s[4:5]
	s_and_b64 vcc, exec, s[2:3]
	s_cbranch_vccnz .LBB0_3431
	s_mov_b32 s2, 24
	s_lshl_b32 s2, s2, 3
	s_add_i32 s2, s2, 0
	s_add_i32 s2, s2, 0x201c0
	v_mov_b32_e32 v0, s2
	s_waitcnt vmcnt(0) lgkmcnt(0)
	ds_read_b32 v1, v0
	ds_read_b32 v0, v0 offset:4
	s_and_b32 s40, s33, 0xffffffc0
	v_mbcnt_lo_u32_b32 v2, -1, 0
	v_mbcnt_hi_u32_b32 v2, -1, v2
	s_waitcnt lgkmcnt(1)
	v_readfirstlane_b32 s18, v1
	s_waitcnt lgkmcnt(0)
	v_readfirstlane_b32 s19, v0
	v_add_u32_e32 v0, s40, v2
	v_cmp_gt_i32_e32 vcc, 64, v0
	s_and_saveexec_b64 s[2:3], vcc
	s_cbranch_execz .LBB0_3329
	v_lshlrev_b32_e32 v2, 5, v0
	v_ashrrev_i32_e32 v3, 31, v2
	v_lshl_add_u64 v[2:3], v[2:3], 2, s[18:19]
	v_add_co_u32_e32 v2, vcc, 0xc000, v2
	v_lshlrev_b32_e32 v9, 2, v0
	s_nop 0
	v_addc_co_u32_e32 v3, vcc, 0, v3, vcc
	global_load_dword v8, v[2:3], off sc1
	v_add_u32_e32 v1, -4, v9
	v_cmp_lt_i32_e32 vcc, 0, v0
	v_add_u32_e32 v4, -8, v9
	v_add_u32_e32 v5, -16, v9
	v_subrev_u32_e32 v6, 32, v9
	v_subrev_u32_e32 v7, 64, v9
	v_add_u32_e32 v10, 0xffffff80, v9
	v_add_u32_e32 v9, 0, v9
	v_add_u32_e32 v9, 0x20a00, v9
	s_waitcnt vmcnt(0)
	v_add_u32_e32 v2, 0xff, v8
	v_ashrrev_i32_e32 v2, 8, v2
	ds_bpermute_b32 v1, v1, v2
	ds_write_b32 v9, v8
	s_waitcnt lgkmcnt(1)
	v_cndmask_b32_e32 v3, 0, v1, vcc
	v_add_u32_e32 v1, v3, v2
	ds_bpermute_b32 v4, v4, v1
	v_cmp_lt_i32_e32 vcc, 1, v0
	s_waitcnt lgkmcnt(0)
	s_nop 0
	v_cndmask_b32_e32 v4, 0, v4, vcc
	v_add_u32_e32 v1, v4, v1
	ds_bpermute_b32 v5, v5, v1
	v_cmp_lt_i32_e32 vcc, 3, v0
	s_waitcnt lgkmcnt(0)
	s_nop 0
	v_cndmask_b32_e32 v5, 0, v5, vcc
	v_add_u32_e32 v1, v5, v1
	ds_bpermute_b32 v6, v6, v1
	v_cmp_lt_i32_e32 vcc, 7, v0
	s_waitcnt lgkmcnt(0)
	s_nop 0
	v_cndmask_b32_e32 v6, 0, v6, vcc
	v_add_u32_e32 v1, v6, v1
	ds_bpermute_b32 v7, v7, v1
	v_cmp_lt_i32_e32 vcc, 15, v0
	s_waitcnt lgkmcnt(0)
	s_nop 0
	v_cndmask_b32_e32 v7, 0, v7, vcc
	v_add_u32_e32 v1, v7, v1
	ds_bpermute_b32 v10, v10, v1
	v_cmp_lt_i32_e32 vcc, 31, v0
	s_waitcnt lgkmcnt(0)
	s_nop 0
	v_cndmask_b32_e32 v9, 0, v10, vcc
	v_cmp_eq_u32_e32 vcc, 63, v0
	s_and_saveexec_b64 s[4:5], vcc
	s_add_i32 s6, 0, 0x20b00
	v_add_u32_e32 v1, v9, v1
	v_mov_b32_e32 v8, s6
	ds_write_b32 v8, v1
	s_or_b64 exec, exec, s[4:5]
	v_cmp_lt_i32_e32 vcc, 0, v2
	s_and_b64 exec, exec, vcc
	s_cbranch_execz .LBB0_3329
	v_lshlrev_b32_e32 v8, 16, v0
	v_cmp_ne_u32_e32 vcc, 1, v2
	s_mov_b64 s[6:7], -1
	v_mov_b32_e32 v0, 0
	s_and_saveexec_b64 s[4:5], vcc
	s_cbranch_execz .LBB0_3326
	v_add_u32_e32 v0, -2, v2
	v_lshrrev_b32_e32 v1, 1, v0
	v_cmp_lt_u32_e32 vcc, 13, v0
	v_mov_b32_e32 v0, 0
	v_add_u32_e32 v10, 1, v1
	s_mov_b32 s14, 0
	v_mov_b32_e32 v1, 1
	v_mov_b32_e32 v13, v0
	s_and_saveexec_b64 s[6:7], vcc
	s_cbranch_execz .LBB0_3322
	v_add_u32_e32 v0, v3, v4
	v_add3_u32 v0, v0, v5, v6
	v_add3_u32 v0, v0, v7, v9
	v_lshl_add_u32 v0, v0, 2, 0
	v_and_b32_e32 v11, -8, v10
	v_add_u32_e32 v12, 0x20400, v0
	s_mov_b32 s13, 1
	s_mov_b64 s[8:9], 0
	s_mov_b32 s12, 0
	.p2align 6

.LBB0_4306:
	s_cmp_gt_i32 s34, 47
	s_cselect_b64 s[2:3], -1, 0
	s_cmp_lt_i32 s35, 48
	s_cselect_b64 s[4:5], -1, 0
	s_or_b64 s[2:3], s[2:3], s[4:5]
	s_and_b64 vcc, exec, s[2:3]
	s_cbranch_vccnz .LBB0_4429
	s_mov_b32 s2, 24
	s_lshl_b32 s2, s2, 3
	s_add_i32 s2, s2, 0
	s_add_i32 s2, s2, 0x201c0
	v_mov_b32_e32 v0, s2
	s_waitcnt vmcnt(0) lgkmcnt(0)
	ds_read_b32 v1, v0
	ds_read_b32 v0, v0 offset:4
	s_and_b32 s42, s33, 0xffffffc0
	v_mbcnt_lo_u32_b32 v2, -1, 0
	v_mbcnt_hi_u32_b32 v2, -1, v2
	s_waitcnt lgkmcnt(1)
	v_readfirstlane_b32 s2, v1
	s_waitcnt lgkmcnt(0)
	v_readfirstlane_b32 s3, v0
	v_add_u32_e32 v0, s42, v2
	v_cmp_gt_i32_e32 vcc, 64, v0
	s_and_saveexec_b64 s[4:5], vcc
	s_cbranch_execz .LBB0_4323
	v_lshlrev_b32_e32 v2, 5, v0
	v_ashrrev_i32_e32 v3, 31, v2
	v_lshl_add_u64 v[2:3], v[2:3], 2, s[2:3]
	v_add_co_u32_e32 v2, vcc, 0xe000, v2
	v_lshlrev_b32_e32 v9, 2, v0
	s_nop 0
	v_addc_co_u32_e32 v3, vcc, 0, v3, vcc
	global_load_dword v8, v[2:3], off sc1
	v_add_u32_e32 v1, -4, v9
	v_cmp_lt_i32_e32 vcc, 0, v0
	v_add_u32_e32 v4, -8, v9
	v_add_u32_e32 v5, -16, v9
	v_subrev_u32_e32 v6, 32, v9
	v_subrev_u32_e32 v7, 64, v9
	v_add_u32_e32 v10, 0xffffff80, v9
	v_add_u32_e32 v9, 0, v9
	v_add_u32_e32 v9, 0x20a00, v9
	s_waitcnt vmcnt(0)
	v_add_u32_e32 v2, 0xff, v8
	v_ashrrev_i32_e32 v2, 8, v2
	ds_bpermute_b32 v1, v1, v2
	ds_write_b32 v9, v8
	s_waitcnt lgkmcnt(1)
	v_cndmask_b32_e32 v3, 0, v1, vcc
	v_add_u32_e32 v1, v3, v2
	ds_bpermute_b32 v4, v4, v1
	v_cmp_lt_i32_e32 vcc, 1, v0
	s_waitcnt lgkmcnt(0)
	s_nop 0
	v_cndmask_b32_e32 v4, 0, v4, vcc
	v_add_u32_e32 v1, v4, v1
	ds_bpermute_b32 v5, v5, v1
	v_cmp_lt_i32_e32 vcc, 3, v0
	s_waitcnt lgkmcnt(0)
	s_nop 0
	v_cndmask_b32_e32 v5, 0, v5, vcc
	v_add_u32_e32 v1, v5, v1
	ds_bpermute_b32 v6, v6, v1
	v_cmp_lt_i32_e32 vcc, 7, v0
	s_waitcnt lgkmcnt(0)
	s_nop 0
	v_cndmask_b32_e32 v6, 0, v6, vcc
	v_add_u32_e32 v1, v6, v1
	ds_bpermute_b32 v7, v7, v1
	v_cmp_lt_i32_e32 vcc, 15, v0
	s_waitcnt lgkmcnt(0)
	s_nop 0
	v_cndmask_b32_e32 v7, 0, v7, vcc
	v_add_u32_e32 v1, v7, v1
	ds_bpermute_b32 v10, v10, v1
	v_cmp_lt_i32_e32 vcc, 31, v0
	s_waitcnt lgkmcnt(0)
	s_nop 0
	v_cndmask_b32_e32 v9, 0, v10, vcc
	v_cmp_eq_u32_e32 vcc, 63, v0
	s_and_saveexec_b64 s[6:7], vcc
	s_add_i32 s8, 0, 0x20b00
	v_add_u32_e32 v1, v9, v1
	v_mov_b32_e32 v8, s8
	ds_write_b32 v8, v1
	s_or_b64 exec, exec, s[6:7]
	v_cmp_lt_i32_e32 vcc, 0, v2
	s_and_b64 exec, exec, vcc
	s_cbranch_execz .LBB0_4323
	v_lshlrev_b32_e32 v8, 16, v0
	v_cmp_ne_u32_e32 vcc, 1, v2
	s_mov_b64 s[8:9], -1
	v_mov_b32_e32 v0, 0
	s_and_saveexec_b64 s[6:7], vcc
	s_cbranch_execz .LBB0_4320
	v_add_u32_e32 v0, -2, v2
	v_lshrrev_b32_e32 v1, 1, v0
	v_cmp_lt_u32_e32 vcc, 13, v0
	v_mov_b32_e32 v0, 0
	v_add_u32_e32 v10, 1, v1
	s_mov_b32 s16, 0
	v_mov_b32_e32 v1, 1
	v_mov_b32_e32 v13, v0
	s_and_saveexec_b64 s[8:9], vcc
	s_cbranch_execz .LBB0_4316
	v_add_u32_e32 v0, v3, v4
	v_add3_u32 v0, v0, v5, v6
	v_add3_u32 v0, v0, v7, v9
	v_lshl_add_u32 v0, v0, 2, 0
	v_and_b32_e32 v11, -8, v10
	v_add_u32_e32 v12, 0x20400, v0
	s_mov_b32 s15, 1
	s_mov_b64 s[12:13], 0
	s_mov_b32 s14, 0
	.p2align 6

.LBB0_4354:
	s_add_u32 s23, s36, 0x100
	s_addc_u32 s65, s37, 0
	s_add_u32 s36, s30, 0x80
	v_mov_b32_e32 v135, v133
	v_mov_b32_e32 v141, v133
	s_addc_u32 s37, s31, 0
	v_mov_b32_e32 v0, 0
	v_lshl_add_u64 v[142:143], s[36:37], 0, v[140:141]
	v_lshl_add_u64 v[144:145], s[36:37], 0, v[134:135]
	s_mov_b32 s66, -2
	s_mov_b64 s[36:37], 0
	v_mov_b32_e32 v1, v0
	v_mov_b32_e32 v2, v0
	v_mov_b32_e32 v3, v0
	v_mov_b32_e32 v4, v0
	v_mov_b32_e32 v5, v0
	v_mov_b32_e32 v6, v0
	v_mov_b32_e32 v7, v0
	v_mov_b32_e32 v16, v0
	v_mov_b32_e32 v17, v0
	v_mov_b32_e32 v18, v0
	v_mov_b32_e32 v19, v0
	v_mov_b32_e32 v20, v0
	v_mov_b32_e32 v21, v0
	v_mov_b32_e32 v22, v0
	v_mov_b32_e32 v23, v0
	v_mov_b32_e32 v32, v0
	v_mov_b32_e32 v33, v0
	v_mov_b32_e32 v34, v0
	v_mov_b32_e32 v35, v0
	v_mov_b32_e32 v36, v0
	v_mov_b32_e32 v37, v0
	v_mov_b32_e32 v38, v0
	v_mov_b32_e32 v39, v0
	v_mov_b32_e32 v48, v0
	v_mov_b32_e32 v49, v0
	v_mov_b32_e32 v50, v0
	v_mov_b32_e32 v51, v0
	v_mov_b32_e32 v52, v0
	v_mov_b32_e32 v53, v0
	v_mov_b32_e32 v54, v0
	v_mov_b32_e32 v55, v0
	v_mov_b32_e32 v8, v0
	v_mov_b32_e32 v9, v0
	v_mov_b32_e32 v10, v0
	v_mov_b32_e32 v11, v0
	v_mov_b32_e32 v12, v0
	v_mov_b32_e32 v13, v0
	v_mov_b32_e32 v14, v0
	v_mov_b32_e32 v15, v0
	v_mov_b32_e32 v24, v0
	v_mov_b32_e32 v25, v0
	v_mov_b32_e32 v26, v0
	v_mov_b32_e32 v27, v0
	v_mov_b32_e32 v28, v0
	v_mov_b32_e32 v29, v0
	v_mov_b32_e32 v30, v0
	v_mov_b32_e32 v31, v0
	v_mov_b32_e32 v40, v0
	v_mov_b32_e32 v41, v0
	v_mov_b32_e32 v42, v0
	v_mov_b32_e32 v43, v0
	v_mov_b32_e32 v44, v0
	v_mov_b32_e32 v45, v0
	v_mov_b32_e32 v46, v0
	v_mov_b32_e32 v47, v0
	v_mov_b32_e32 v56, v0
	v_mov_b32_e32 v57, v0
	v_mov_b32_e32 v58, v0
	v_mov_b32_e32 v59, v0
	v_mov_b32_e32 v60, v0
	v_mov_b32_e32 v61, v0
	v_mov_b32_e32 v62, v0
	v_mov_b32_e32 v63, v0
	v_mov_b32_e32 v64, v0
	v_mov_b32_e32 v65, v0
	v_mov_b32_e32 v66, v0
	v_mov_b32_e32 v67, v0
	v_mov_b32_e32 v68, v0
	v_mov_b32_e32 v69, v0
	v_mov_b32_e32 v70, v0
	v_mov_b32_e32 v71, v0
	v_mov_b32_e32 v80, v0
	v_mov_b32_e32 v81, v0
	v_mov_b32_e32 v82, v0
	v_mov_b32_e32 v83, v0
	v_mov_b32_e32 v84, v0
	v_mov_b32_e32 v85, v0
	v_mov_b32_e32 v86, v0
	v_mov_b32_e32 v87, v0
	v_mov_b32_e32 v96, v0
	v_mov_b32_e32 v97, v0
	v_mov_b32_e32 v98, v0
	v_mov_b32_e32 v99, v0
	v_mov_b32_e32 v100, v0
	v_mov_b32_e32 v101, v0
	v_mov_b32_e32 v102, v0
	v_mov_b32_e32 v103, v0
	v_mov_b32_e32 v120, v0
	v_mov_b32_e32 v121, v0
	v_mov_b32_e32 v122, v0
	v_mov_b32_e32 v123, v0
	v_mov_b32_e32 v124, v0
	v_mov_b32_e32 v125, v0
	v_mov_b32_e32 v126, v0
	v_mov_b32_e32 v127, v0
	v_mov_b32_e32 v72, v0
	v_mov_b32_e32 v73, v0
	v_mov_b32_e32 v74, v0
	v_mov_b32_e32 v75, v0
	v_mov_b32_e32 v76, v0
	v_mov_b32_e32 v77, v0
	v_mov_b32_e32 v78, v0
	v_mov_b32_e32 v79, v0
	v_mov_b32_e32 v88, v0
	v_mov_b32_e32 v89, v0
	v_mov_b32_e32 v90, v0
	v_mov_b32_e32 v91, v0
	v_mov_b32_e32 v92, v0
	v_mov_b32_e32 v93, v0
	v_mov_b32_e32 v94, v0
	v_mov_b32_e32 v95, v0
	v_mov_b32_e32 v104, v0
	v_mov_b32_e32 v105, v0
	v_mov_b32_e32 v106, v0
	v_mov_b32_e32 v107, v0
	v_mov_b32_e32 v108, v0
	v_mov_b32_e32 v109, v0
	v_mov_b32_e32 v110, v0
	v_mov_b32_e32 v111, v0
	v_mov_b32_e32 v112, v0
	v_mov_b32_e32 v113, v0
	v_mov_b32_e32 v114, v0
	v_mov_b32_e32 v115, v0
	v_mov_b32_e32 v116, v0
	v_mov_b32_e32 v117, v0
	v_mov_b32_e32 v118, v0
	v_mov_b32_e32 v119, v0
	.p2align 6

.LBB0_4429:
	s_cmp_gt_i32 s34, 48
	s_cselect_b64 s[2:3], -1, 0
	s_cmp_lt_i32 s35, 49
	s_cselect_b64 s[4:5], -1, 0
	s_or_b64 s[2:3], s[2:3], s[4:5]
	s_and_b64 vcc, exec, s[2:3]
	s_cbranch_vccnz .LBB0_4548
	s_mov_b32 s2, 24
	s_lshl_b32 s2, s2, 3
	s_add_i32 s2, s2, 0
	s_add_i32 s2, s2, 0x201c0
	v_mov_b32_e32 v0, s2
	s_waitcnt vmcnt(0) lgkmcnt(0)
	ds_read_b32 v1, v0
	ds_read_b32 v0, v0 offset:4
	s_andn2_b32 s33, s33, 63
	v_mbcnt_lo_u32_b32 v2, -1, 0
	v_mbcnt_hi_u32_b32 v2, -1, v2
	s_waitcnt lgkmcnt(1)
	v_readfirstlane_b32 s18, v1
	s_waitcnt lgkmcnt(0)
	v_readfirstlane_b32 s19, v0
	v_add_u32_e32 v0, s33, v2
	v_cmp_gt_i32_e32 vcc, 64, v0
	s_and_saveexec_b64 s[2:3], vcc
	s_cbranch_execz .LBB0_4446
	v_lshlrev_b32_e32 v2, 5, v0
	v_ashrrev_i32_e32 v3, 31, v2
	v_lshl_add_u64 v[2:3], v[2:3], 2, s[18:19]
	v_add_co_u32_e32 v2, vcc, 0xe000, v2
	v_lshlrev_b32_e32 v9, 2, v0
	s_nop 0
	v_addc_co_u32_e32 v3, vcc, 0, v3, vcc
	global_load_dword v8, v[2:3], off sc1
	v_add_u32_e32 v1, -4, v9
	v_cmp_lt_i32_e32 vcc, 0, v0
	v_add_u32_e32 v4, -8, v9
	v_add_u32_e32 v5, -16, v9
	v_subrev_u32_e32 v6, 32, v9
	v_subrev_u32_e32 v7, 64, v9
	v_add_u32_e32 v10, 0xffffff80, v9
	v_add_u32_e32 v9, 0, v9
	v_add_u32_e32 v9, 0x20a00, v9
	s_waitcnt vmcnt(0)
	v_add_u32_e32 v2, 0xff, v8
	v_ashrrev_i32_e32 v2, 8, v2
	ds_bpermute_b32 v1, v1, v2
	ds_write_b32 v9, v8
	s_waitcnt lgkmcnt(1)
	v_cndmask_b32_e32 v3, 0, v1, vcc
	v_add_u32_e32 v1, v3, v2
	ds_bpermute_b32 v4, v4, v1
	v_cmp_lt_i32_e32 vcc, 1, v0
	s_waitcnt lgkmcnt(0)
	s_nop 0
	v_cndmask_b32_e32 v4, 0, v4, vcc
	v_add_u32_e32 v1, v4, v1
	ds_bpermute_b32 v5, v5, v1
	v_cmp_lt_i32_e32 vcc, 3, v0
	s_waitcnt lgkmcnt(0)
	s_nop 0
	v_cndmask_b32_e32 v5, 0, v5, vcc
	v_add_u32_e32 v1, v5, v1
	ds_bpermute_b32 v6, v6, v1
	v_cmp_lt_i32_e32 vcc, 7, v0
	s_waitcnt lgkmcnt(0)
	s_nop 0
	v_cndmask_b32_e32 v6, 0, v6, vcc
	v_add_u32_e32 v1, v6, v1
	ds_bpermute_b32 v7, v7, v1
	v_cmp_lt_i32_e32 vcc, 15, v0
	s_waitcnt lgkmcnt(0)
	s_nop 0
	v_cndmask_b32_e32 v7, 0, v7, vcc
	v_add_u32_e32 v1, v7, v1
	ds_bpermute_b32 v10, v10, v1
	v_cmp_lt_i32_e32 vcc, 31, v0
	s_waitcnt lgkmcnt(0)
	s_nop 0
	v_cndmask_b32_e32 v9, 0, v10, vcc
	v_cmp_eq_u32_e32 vcc, 63, v0
	s_and_saveexec_b64 s[4:5], vcc
	s_add_i32 s6, 0, 0x20b00
	v_add_u32_e32 v1, v9, v1
	v_mov_b32_e32 v8, s6
	ds_write_b32 v8, v1
	s_or_b64 exec, exec, s[4:5]
	v_cmp_lt_i32_e32 vcc, 0, v2
	s_and_b64 exec, exec, vcc
	s_cbranch_execz .LBB0_4446
	v_lshlrev_b32_e32 v8, 16, v0
	v_cmp_ne_u32_e32 vcc, 1, v2
	s_mov_b64 s[6:7], -1
	v_mov_b32_e32 v0, 0
	s_and_saveexec_b64 s[4:5], vcc
	s_cbranch_execz .LBB0_4443
	v_add_u32_e32 v0, -2, v2
	v_lshrrev_b32_e32 v1, 1, v0
	v_cmp_lt_u32_e32 vcc, 13, v0
	v_mov_b32_e32 v0, 0
	v_add_u32_e32 v10, 1, v1
	s_mov_b32 s14, 0
	v_mov_b32_e32 v1, 1
	v_mov_b32_e32 v13, v0
	s_and_saveexec_b64 s[6:7], vcc
	s_cbranch_execz .LBB0_4439
	v_add_u32_e32 v0, v3, v4
	v_add3_u32 v0, v0, v5, v6
	v_add3_u32 v0, v0, v7, v9
	v_lshl_add_u32 v0, v0, 2, 0
	v_and_b32_e32 v11, -8, v10
	v_add_u32_e32 v12, 0x20400, v0
	s_mov_b32 s13, 1
	s_mov_b64 s[8:9], 0
	s_mov_b32 s12, 0
	.p2align 6

.LBB0_4456:
	s_and_b64 vcc, exec, s[30:31]
	s_mov_b32 s51, s65
	s_mov_b32 s48, s64
	s_mov_b32 s66, s63
	s_mov_b64 s[38:39], s[28:29]
	s_mov_b64 s[36:37], s[26:27]
	s_cbranch_vccnz .LBB0_4480
	.p2align 6

.LBB0_4552:
	s_lshl_b32 s0, s4, 3
	s_add_i32 s0, s0, s11
	s_cmpk_gt_i32 s0, 0x7fff
	v_mbcnt_lo_u32_b32 v0, -1, 0
	v_mbcnt_hi_u32_b32 v0, -1, v0
	s_cbranch_scc1 .LBB0_4555
	v_and_b32_e32 v6, 63, v0
	v_lshlrev_b32_e32 v4, 2, v6
	v_mov_b32_e32 v5, 0
	s_lshl_b32 s1, s4, 4
	s_lshl_b32 s4, s11, 1
	v_lshl_add_u64 v[0:1], s[6:7], 0, v[4:5]
	s_mov_b64 s[12:13], 0x38000000
	s_add_i32 s4, s1, s4
	s_ashr_i32 s1, s0, 31
	s_lshl_b32 s2, s3, 3
	v_lshl_add_u64 v[0:1], v[0:1], 0, s[12:13]
	s_lshl_b32 s11, s3, 4
	s_lshl_b64 s[12:13], s[0:1], 11
	s_add_u32 s6, s6, s12
	v_lshlrev_b32_e32 v4, 3, v6
	s_addc_u32 s7, s7, s13
	v_lshl_add_u64 v[2:3], s[6:7], 0, v[4:5]
	s_mov_b64 s[6:7], 0x26000000
	s_ashr_i32 s3, s2, 31
	v_lshl_add_u64 v[2:3], v[2:3], 0, s[6:7]
	s_lshl_b64 s[6:7], s[2:3], 11
	s_lshl_b64 s[12:13], s[0:1], 12
	s_add_u32 s12, s5, s12
	v_lshlrev_b32_e32 v4, 4, v6
	s_addc_u32 s13, s8, s13
	v_lshl_add_u64 v[4:5], s[12:13], 0, v[4:5]
	s_mov_b64 s[8:9], 0xc00
	v_lshl_add_u64 v[4:5], v[4:5], 0, s[8:9]
	s_lshl_b64 s[8:9], s[2:3], 12
	s_mov_b32 s10, 0x3d800000
	.p2align 6
